# NSA: half-wave (lane^32) row-max/row-sum exchanges via v_permlane32_swap instead of ds_bpermute at 9 sites; on top of router loop rewrite
# speedup vs baseline: 1.0077x; 1.0053x over previous
; #define GAS __attribute__((address_space(1)))
; #define LAS __attribute__((address_space(3)))
; __device__ __forceinline__ void nsa_mfma_phase(Frame& F, int l, bf16* YC, int ypitch) {
;     ...
;         u32x4 qv4[4]; float kmx_ = 0.f; unsigned short g0_, g1_h, g2_h;
;         { int hq = lane; asm volatile("" : "+v"(hq)); const bf16* qp = Z + NSA_ROW() * NZ + Z_Q + head * 64 + 8 * (hq >> 5);
; #pragma unroll
;           for (int ks = 0; ks < 4; ++ks) qv4[ks] = *(const GAS u32x4*)(qp + 16 * ks);
;           int tk = tid; asm volatile("" : "+v"(tk)); if (tk < 128) kmx_ = *(const GAS float*)((const float*)(F.ws + WS_KMX) + (((tk >> 6) * BATCH + b) * NG + g) * 64 + (tk & 63));
;           const bf16* gp = Z + NSA_ROW() * NZ + Z_NG + head * 3; g0_ = *(const GAS unsigned short*)(gp); g1_h = *(const GAS unsigned short*)(gp + 1); g2_h = *(const GAS unsigned short*)(gp + 2); }
; #pragma unroll
;         for (int ks = 0; ks < 4; ++ks) { const u32x4 qv = qv4[ks];
;             u32x4 qs; qs.x = cvtpk(bflo(qv.x) * scale2, bfhi(qv.x) * scale2); qs.y = cvtpk(bflo(qv.y) * scale2, bfhi(qv.y) * scale2); qs.z = cvtpk(bflo(qv.z) * scale2, bfhi(qv.z) * scale2); qs.w = cvtpk(bflo(qv.w) * scale2, bfhi(qv.w) * scale2);
;             qf[ks] = __builtin_bit_cast(bf16x8, qs); }
;         f32x16 o[2];
;         const bf16* zb = Z + (size_t)b * SEQ * NZ;
;         { float ss = 0.f;
; #pragma unroll
;             for (int ks = 0; ks < 4; ++ks) { const u32x4 qq = __builtin_bit_cast(u32x4, qf[ks]); ss += bflo(qq.x) * bflo(qq.x) + bfhi(qq.x) * bfhi(qq.x) + bflo(qq.y) * bflo(qq.y) + bfhi(qq.y) * bfhi(qq.y) + bflo(qq.z) * bflo(qq.z) + bfhi(qq.z) * bfhi(qq.z) + bflo(qq.w) * bflo(qq.w) + bfhi(qq.w) * bfhi(qq.w); }
;             ss += __shfl_xor(ss, 32); ((LAS float*)(lds + L_QN))[w * 64 + lane] = sqrtf(ss) * 1.001f;
;             int tk = tid; asm volatile("" : "+v"(tk)); if (tk < 128) ((LAS float*)(lds + L_KMX))[tk] = kmx_; }
;         { int lg_ = lane; asm volatile("" : "+v"(lg_)); LAS float* gt = (LAS float*)(lds + L_GT) + w * 192 + lg_;
;             gt[0] = sigmoidf_(__builtin_bit_cast(float, (unsigned)g0_ << 16)); gt[64] = sigmoidf_(__builtin_bit_cast(float, (unsigned)g1_h << 16)); gt[128] = sigmoidf_(__builtin_bit_cast(float, (unsigned)g2_h << 16)); }
;         { int ti = tid; asm volatile("" : "+v"(ti)); for (int i = ti; i < 4 * 64 * 65; i += NTHR) IMP[i] = 0.f; }
.LBB0_477:
	s_or_b64 exec, exec, s[0:1]
	v_mov_b32_e32 v18, v123
	s_nop 0
	v_and_or_b32 v20, v18, 31, s69
	v_mov_b64_e32 v[18:19], s[50:51]
	v_mad_u64_u32 v[18:19], s[0:1], v20, s33, v[18:19]
	s_mul_i32 s0, s5, 3
	s_ashr_i32 s1, s0, 31
	v_lshl_add_u64 v[18:19], s[0:1], 1, v[18:19]
	s_mov_b64 s[0:1], 0x3c00
	v_lshl_add_u64 v[20:21], v[18:19], 0, s[0:1]
	v_add_co_u32_e32 v18, vcc, 0x3000, v18
	s_mov_b32 s0, 0x3e38aa3b
	s_nop 0
	v_addc_co_u32_e32 v19, vcc, 0, v19, vcc
	global_load_dword v19, v[18:19], off offset:3072
	s_nop 0
	global_load_ushort v18, v[20:21], off offset:4
	s_waitcnt vmcnt(0)
	v_lshlrev_b32_e32 v20, 16, v14
	v_and_b32_e32 v21, 0xffff0000, v14
	v_lshlrev_b32_e32 v14, 16, v15
	v_and_b32_e32 v15, 0xffff0000, v15
	v_pk_mul_f32 v[14:15], v[14:15], s[0:1] op_sel_hi:[1,0]
	v_pk_mul_f32 v[20:21], v[20:21], s[0:1] op_sel_hi:[1,0]
	v_cvt_pk_bf16_f32 v99, v14, v15
	v_lshlrev_b32_e32 v14, 16, v16
	v_and_b32_e32 v15, 0xffff0000, v16
	v_pk_mul_f32 v[14:15], v[14:15], s[0:1] op_sel_hi:[1,0]
	v_cvt_pk_bf16_f32 v98, v20, v21
	v_cvt_pk_bf16_f32 v100, v14, v15
	v_lshlrev_b32_e32 v14, 16, v17
	v_and_b32_e32 v15, 0xffff0000, v17
	v_pk_mul_f32 v[14:15], v[14:15], s[0:1] op_sel_hi:[1,0]
	s_nop 0
	v_cvt_pk_bf16_f32 v101, v14, v15
	v_lshlrev_b32_e32 v14, 16, v10
	v_and_b32_e32 v15, 0xffff0000, v10
	v_lshlrev_b32_e32 v10, 16, v11
	v_and_b32_e32 v11, 0xffff0000, v11
	v_pk_mul_f32 v[10:11], v[10:11], s[0:1] op_sel_hi:[1,0]
	v_pk_mul_f32 v[14:15], v[14:15], s[0:1] op_sel_hi:[1,0]
	v_cvt_pk_bf16_f32 v103, v10, v11
	v_lshlrev_b32_e32 v10, 16, v12
	v_and_b32_e32 v11, 0xffff0000, v12
	v_pk_mul_f32 v[10:11], v[10:11], s[0:1] op_sel_hi:[1,0]
	v_cvt_pk_bf16_f32 v102, v14, v15
	v_cvt_pk_bf16_f32 v104, v10, v11
	v_lshlrev_b32_e32 v10, 16, v13
	v_and_b32_e32 v11, 0xffff0000, v13
	v_pk_mul_f32 v[10:11], v[10:11], s[0:1] op_sel_hi:[1,0]
	s_nop 0
	v_cvt_pk_bf16_f32 v105, v10, v11
	v_lshlrev_b32_e32 v10, 16, v6
	v_and_b32_e32 v11, 0xffff0000, v6
	v_lshlrev_b32_e32 v6, 16, v7
	v_and_b32_e32 v7, 0xffff0000, v7
	v_pk_mul_f32 v[6:7], v[6:7], s[0:1] op_sel_hi:[1,0]
	v_pk_mul_f32 v[10:11], v[10:11], s[0:1] op_sel_hi:[1,0]
	v_cvt_pk_bf16_f32 v107, v6, v7
	v_lshlrev_b32_e32 v6, 16, v8
	v_and_b32_e32 v7, 0xffff0000, v8
	v_pk_mul_f32 v[6:7], v[6:7], s[0:1] op_sel_hi:[1,0]
	v_cvt_pk_bf16_f32 v106, v10, v11
	v_cvt_pk_bf16_f32 v108, v6, v7
	v_lshlrev_b32_e32 v6, 16, v9
	v_and_b32_e32 v7, 0xffff0000, v9
	v_pk_mul_f32 v[6:7], v[6:7], s[0:1] op_sel_hi:[1,0]
	s_nop 0
	v_cvt_pk_bf16_f32 v109, v6, v7
	s_waitcnt vmcnt(2)
	v_lshlrev_b32_e32 v6, 16, v2
	v_and_b32_e32 v7, 0xffff0000, v2
	v_lshlrev_b32_e32 v2, 16, v3
	v_and_b32_e32 v3, 0xffff0000, v3
	v_pk_mul_f32 v[2:3], v[2:3], s[0:1] op_sel_hi:[1,0]
	v_pk_mul_f32 v[6:7], v[6:7], s[0:1] op_sel_hi:[1,0]
	v_cvt_pk_bf16_f32 v111, v2, v3
	v_lshlrev_b32_e32 v2, 16, v4
	v_and_b32_e32 v3, 0xffff0000, v4
	v_pk_mul_f32 v[2:3], v[2:3], s[0:1] op_sel_hi:[1,0]
	v_and_b32_e32 v4, 0xffff0000, v98
	v_cvt_pk_bf16_f32 v112, v2, v3
	v_lshlrev_b32_e32 v2, 16, v5
	v_and_b32_e32 v3, 0xffff0000, v5
	v_pk_mul_f32 v[2:3], v[2:3], s[0:1] op_sel_hi:[1,0]
	v_and_b32_e32 v5, 0xffff0000, v102
	v_cvt_pk_bf16_f32 v113, v2, v3
	v_lshlrev_b32_e32 v3, 16, v102
	v_lshlrev_b32_e32 v2, 16, v98
	v_pk_mul_f32 v[4:5], v[4:5], v[4:5]
	v_cvt_pk_bf16_f32 v110, v6, v7
	v_pk_fma_f32 v[2:3], v[2:3], v[2:3], v[4:5]
	v_lshlrev_b32_e32 v5, 16, v103
	v_lshlrev_b32_e32 v4, 16, v99
	v_pk_fma_f32 v[2:3], v[4:5], v[4:5], v[2:3]
	v_and_b32_e32 v5, 0xffff0000, v103
	v_and_b32_e32 v4, 0xffff0000, v99
	v_pk_fma_f32 v[2:3], v[4:5], v[4:5], v[2:3]
	v_lshlrev_b32_e32 v5, 16, v104
	v_lshlrev_b32_e32 v4, 16, v100
	v_pk_fma_f32 v[2:3], v[4:5], v[4:5], v[2:3]
	v_and_b32_e32 v5, 0xffff0000, v104
	v_and_b32_e32 v4, 0xffff0000, v100
	v_pk_fma_f32 v[2:3], v[4:5], v[4:5], v[2:3]
	v_lshlrev_b32_e32 v5, 16, v105
	v_lshlrev_b32_e32 v4, 16, v101
	v_pk_fma_f32 v[2:3], v[4:5], v[4:5], v[2:3]
	v_and_b32_e32 v5, 0xffff0000, v105
	v_and_b32_e32 v4, 0xffff0000, v101
	v_and_b32_e32 v7, 0xffff0000, v110
	v_and_b32_e32 v6, 0xffff0000, v106
	v_pk_fma_f32 v[2:3], v[4:5], v[4:5], v[2:3]
	v_lshlrev_b32_e32 v5, 16, v110
	v_lshlrev_b32_e32 v4, 16, v106
	v_pk_mul_f32 v[6:7], v[6:7], v[6:7]
	v_add_f32_e32 v2, v2, v3
	v_pk_fma_f32 v[4:5], v[4:5], v[4:5], v[6:7]
	v_lshlrev_b32_e32 v7, 16, v111
	v_lshlrev_b32_e32 v6, 16, v107
	v_pk_fma_f32 v[4:5], v[6:7], v[6:7], v[4:5]
	v_and_b32_e32 v7, 0xffff0000, v111
	v_and_b32_e32 v6, 0xffff0000, v107
	v_pk_fma_f32 v[4:5], v[6:7], v[6:7], v[4:5]
	v_lshlrev_b32_e32 v7, 16, v112
	v_lshlrev_b32_e32 v6, 16, v108
	v_pk_fma_f32 v[4:5], v[6:7], v[6:7], v[4:5]
	v_and_b32_e32 v7, 0xffff0000, v112
	v_and_b32_e32 v6, 0xffff0000, v108
	v_pk_fma_f32 v[4:5], v[6:7], v[6:7], v[4:5]
	v_lshlrev_b32_e32 v7, 16, v113
	v_lshlrev_b32_e32 v6, 16, v109
	v_pk_fma_f32 v[4:5], v[6:7], v[6:7], v[4:5]
	v_and_b32_e32 v7, 0xffff0000, v113
	v_and_b32_e32 v6, 0xffff0000, v109
	v_pk_fma_f32 v[4:5], v[6:7], v[6:7], v[4:5]
	v_xor_b32_e32 v3, 32, v228
	v_add_f32_e32 v2, v2, v4
	v_and_b32_e32 v4, 64, v228
	v_add_u32_e32 v90, 64, v4
	v_cmp_lt_i32_e32 vcc, v3, v90
	v_add_f32_e32 v2, v2, v5
	s_mov_b32 s0, 0xf800000
	v_cndmask_b32_e32 v3, v228, v3, vcc
	v_lshlrev_b32_e32 v115, 2, v3
	v_mov_b32_e32 v3, v2
	s_nop 1
	v_permlane32_swap_b32_e32 v2, v3
	s_waitcnt lgkmcnt(0)
	v_add_f32_e32 v2, v2, v3
	v_mul_f32_e32 v3, 0x4f800000, v2
	v_cmp_gt_f32_e32 vcc, s0, v2
	s_nop 1
	v_cndmask_b32_e32 v2, v2, v3, vcc
	v_sqrt_f32_e32 v3, v2
	s_nop 0
	v_add_u32_e32 v4, -1, v3
	v_fma_f32 v5, -v4, v3, v2
	v_cmp_ge_f32_e64 s[0:1], 0, v5
	v_add_u32_e32 v5, 1, v3
	s_nop 0
	v_cndmask_b32_e64 v4, v3, v4, s[0:1]
	v_fma_f32 v3, -v5, v3, v2
	v_cmp_lt_f32_e64 s[0:1], 0, v3
	s_nop 1
	v_cndmask_b32_e64 v3, v4, v5, s[0:1]
	v_mul_f32_e32 v4, 0x37800000, v3
	v_cndmask_b32_e32 v3, v3, v4, vcc
	v_cmp_class_f32_e32 vcc, v2, v227
	s_movk_i32 s0, 0x80
	s_nop 0
	v_cndmask_b32_e32 v2, v3, v2, vcc
	v_mul_f32_e32 v2, 0x3f8020c5, v2
	ds_write_b32 v127, v2
	v_mov_b32_e32 v2, v122
	s_nop 0
	v_cmp_gt_i32_e32 vcc, s0, v2
	s_and_saveexec_b64 s[0:1], vcc
	v_lshl_add_u32 v2, v2, 2, 0
	v_add_u32_e32 v2, 0x1c600, v2
	ds_write_b32 v2, v0
	s_or_b64 exec, exec, s[0:1]
	s_waitcnt vmcnt(1)
	v_lshlrev_b32_e32 v0, 16, v19
	v_and_b32_e32 v3, 0xffff0000, v19
	v_mul_f32_e32 v0, 0xbfb8aa3b, v0
	v_mul_f32_e32 v3, 0xbfb8aa3b, v3
	s_waitcnt vmcnt(0)
	v_lshlrev_b32_e32 v4, 16, v18
	v_exp_f32_e32 v0, v0
	v_exp_f32_e32 v3, v3
	v_mul_f32_e32 v4, 0xbfb8aa3b, v4
	v_exp_f32_e32 v4, v4
	v_add_f32_e32 v0, 1.0, v0
	v_add_f32_e32 v3, 1.0, v3
	v_rcp_f32_e32 v0, v0
	v_rcp_f32_e32 v3, v3
	v_add_f32_e32 v4, 1.0, v4
	v_mov_b32_e32 v2, v123
	v_rcp_f32_e32 v4, v4
	s_movk_i32 s0, 0x4100
	v_lshl_add_u32 v2, v2, 2, s73
	ds_write2st64_b32 v2, v0, v3 offset1:1
	ds_write_b32 v2, v4 offset:512
	v_mov_b32_e32 v2, v122
	s_nop 0
	v_cmp_gt_i32_e32 vcc, s0, v2
	s_and_saveexec_b64 s[0:1], vcc
	s_cbranch_execz .LBB0_482
	s_add_i32 s2, 0, 0xc000
	v_lshl_add_u32 v0, v2, 2, s2
	v_add_u32_e32 v2, 0xfffffe00, v2
	s_mov_b64 s[2:3], 0

; #define LAS __attribute__((address_space(3)))
; #define MFMA32(a, b, c) __builtin_amdgcn_mfma_f32_32x32x16_bf16((a), (b), (c), 0, 0, 0)
; template <int MODE, int MK  , bool FIRST, class ValidF> ...
;     int ln = L.lane; asm volatile("" : "+v"(ln));
;     const int r32 = ln & 31, hh = ln >> 5;
;     unsigned kofs[4], vofs[2];
; #pragma unroll
;     for (int ks = 0; ks < 4; ++ks) kofs[ks] = (unsigned)(r32 * 128 + (((2 * ks + hh) ^ (r32 & 7)) << 4));
;     { const int q4 = (ln & 15) >> 2, p4 = ln & 3, blk = (ln >> 4) & 1, cc0 = 2 * blk + (p4 >> 1), kk = 4 * hh + q4;
; #pragma unroll
;         for (int dt = 0; dt < 2; ++dt) vofs[dt] = (unsigned)((4 * hh + q4) * 128 + (((cc0 + 4 * dt) ^ kk) << 4) + 8 * (p4 & 1)); }
;     f32x16 p[2];
;     const float cref = c0 + sbk * (float)(4 * hh) - ((MODE == 2 && !FIRST) || MODE == 1 ? m : 0.f);
; #pragma unroll
;     for (int mt = 0; mt < 2; ++mt)
; #pragma unroll
;         for (int r = 0; r < 16; ++r) p[mt][r] = fmaf(sbk, (float)(32 * mt + (r & 3) + 8 * (r >> 2)), cref);
; #pragma unroll
;     for (int ks = 0; ks < 4; ++ks)
; #pragma unroll
;         for (int mt = 0; mt < 2; ++mt) { const bf16x8 a = *(const LAS bf16x8*)(Kb + kofs[ks] + mt * 4096); p[mt] = MFMA32(a, qf[ks], p[mt]); }
;     if (MK != 0) {
; #pragma unroll
;         for (int mt = 0; mt < 2; ++mt)
; #pragma unroll
;             for (int r = 0; r < 16; ++r) { const int kc = 32 * mt + (r & 3) + 8 * (r >> 2); const bool ok = (MK == 2) ? valid(kc + 4 * hh) : lv; p[mt][r] = ok ? p[mt][r] : -INFINITY; } }
.LBB0_487:
	v_mov_b32_e32 v34, v123
	s_add_i32 s9, s47, 0
	v_ashrrev_i32_e32 v35, 5, v34
	v_lshlrev_b32_e32 v36, 7, v34
	v_and_b32_e32 v72, 0xf80, v36
	v_bitop3_b32 v36, v35, v34, 7 bitop3:0x78
	s_nop 3
	v_lshlrev_b32_e32 v50, 4, v36
	s_add_i32 s9, s9, s43
	v_add3_u32 v54, v72, v50, s9
	v_add_u32_e32 v36, 2, v35
	ds_read_b128 v[50:53], v54
	ds_read_b128 v[66:69], v54 offset:4096
	v_bitop3_b32 v36, v36, v34, 7 bitop3:0x78
	v_lshlrev_b32_e32 v76, 2, v35
	v_lshlrev_b32_e32 v73, 4, v36
	v_add_u32_e32 v36, 4, v35
	v_cvt_f32_i32_e32 v89, v76
	v_bitop3_b32 v36, v36, v34, 7 bitop3:0x78
	v_lshlrev_b32_e32 v74, 4, v36
	v_add_u32_e32 v36, 6, v35
	v_bitop3_b32 v34, v36, v34, 7 bitop3:0x78
	v_lshlrev_b32_e32 v75, 4, v34
	v_mul_f32_e32 v34, v82, v89
	v_pk_fma_f32 v[70:71], v[84:85], v[88:89], v[34:35] op_sel_hi:[1,1,0]
	v_mov_b32_e32 v83, v82
	v_fma_f32 v34, 0, v82, v70
	v_add_f32_e32 v35, v82, v70
	v_pk_fma_f32 v[36:37], v[84:85], s[18:19], v[70:71] op_sel_hi:[1,1,0]
	v_pk_fma_f32 v[38:39], v[84:85], s[74:75], v[70:71] op_sel_hi:[1,1,0]
	v_pk_fma_f32 v[40:41], v[84:85], s[36:37], v[70:71] op_sel_hi:[1,1,0]
	v_pk_fma_f32 v[42:43], v[84:85], s[26:27], v[70:71] op_sel_hi:[1,1,0]
	v_pk_fma_f32 v[44:45], v[84:85], s[56:57], v[70:71] op_sel_hi:[1,1,0]
	v_pk_fma_f32 v[46:47], v[84:85], s[22:23], v[70:71] op_sel_hi:[1,1,0]
	v_pk_fma_f32 v[48:49], v[84:85], s[24:25], v[70:71] op_sel_hi:[1,1,0]
	v_pk_fma_f32 v[64:65], v[82:83], s[30:31], v[70:71] op_sel_hi:[1,1,0]
	v_pk_fma_f32 v[62:63], v[82:83], s[20:21], v[70:71] op_sel_hi:[1,1,0]
	s_waitcnt lgkmcnt(1)
	v_mfma_f32_32x32x16_bf16 v[34:49], v[50:53], v[98:101], v[34:49]
	v_fma_f32 v60, v82, s34, v70
	v_fma_f32 v61, v83, s35, v70
	v_fma_f32 v58, v82, s80, v70
	v_fma_f32 v59, v83, s81, v70
	v_fma_f32 v56, v82, s76, v70
	v_fma_f32 v57, v83, s77, v70
	v_pk_fma_f32 v[54:55], v[82:83], s[82:83], v[70:71] op_sel_hi:[1,1,0]
	v_pk_fma_f32 v[52:53], v[82:83], s[84:85], v[70:71] op_sel_hi:[1,1,0]
	v_pk_fma_f32 v[50:51], v[86:87], s[86:87], v[70:71] op_sel_hi:[1,1,0]
	v_add3_u32 v70, v72, v73, s9
	s_waitcnt lgkmcnt(0)
	v_mfma_f32_32x32x16_bf16 v[50:65], v[66:69], v[98:101], v[50:65]
	ds_read_b128 v[66:69], v70
	s_waitcnt lgkmcnt(0)
	v_mfma_f32_32x32x16_bf16 v[34:49], v[66:69], v[102:105], v[34:49]
	ds_read_b128 v[66:69], v70 offset:4096
	v_add3_u32 v70, v72, v74, s9
	s_waitcnt lgkmcnt(0)
	v_mfma_f32_32x32x16_bf16 v[50:65], v[66:69], v[102:105], v[50:65]
	ds_read_b128 v[66:69], v70
	s_waitcnt lgkmcnt(0)
	v_mfma_f32_32x32x16_bf16 v[34:49], v[66:69], v[106:109], v[34:49]
	ds_read_b128 v[66:69], v70 offset:4096
	v_add3_u32 v70, v72, v75, s9
	s_waitcnt lgkmcnt(0)
	v_mfma_f32_32x32x16_bf16 v[50:65], v[66:69], v[106:109], v[50:65]
	ds_read_b128 v[66:69], v70
	s_waitcnt lgkmcnt(0)
	v_mfma_f32_32x32x16_bf16 v[34:49], v[66:69], v[110:113], v[34:49]
	ds_read_b128 v[66:69], v70 offset:4096
	s_waitcnt lgkmcnt(0)
	v_mfma_f32_32x32x16_bf16 v[50:65], v[66:69], v[110:113], v[50:65]
	v_add_u32_e32 v66, s8, v76
	v_cmp_lt_i32_e32 vcc, v66, v0
	v_add_u32_e32 v67, 1, v66
	s_nop 5
	v_cndmask_b32_e32 v34, v233, v34, vcc
	v_cmp_lt_i32_e32 vcc, v67, v0
	v_add_u32_e32 v67, 2, v66
	s_nop 0
	v_cndmask_b32_e32 v35, v233, v35, vcc
	v_cmp_lt_i32_e32 vcc, v67, v0
	v_add_u32_e32 v67, 3, v66
	s_nop 0
	v_cndmask_b32_e32 v36, v233, v36, vcc
	v_cmp_lt_i32_e32 vcc, v67, v0
	v_add_u32_e32 v67, 8, v66
	s_nop 0
	v_cndmask_b32_e32 v37, v233, v37, vcc
	v_cmp_lt_i32_e32 vcc, v67, v0
	v_add_u32_e32 v67, 9, v66
	v_max_f32_e32 v68, v37, v37
	v_cndmask_b32_e32 v38, v233, v38, vcc
	v_cmp_lt_i32_e32 vcc, v67, v0
	v_add_u32_e32 v67, 10, v66
	s_nop 0
	v_cndmask_b32_e32 v39, v233, v39, vcc
	v_cmp_lt_i32_e32 vcc, v67, v0
	v_add_u32_e32 v67, 11, v66
	s_nop 0
	v_cndmask_b32_e32 v40, v233, v40, vcc
	v_cmp_lt_i32_e32 vcc, v67, v0
	v_add_u32_e32 v67, 16, v66
	s_nop 0
	v_cndmask_b32_e32 v41, v233, v41, vcc
	v_cmp_lt_i32_e32 vcc, v67, v0
	v_add_u32_e32 v67, 17, v66
	s_nop 0
	v_cndmask_b32_e32 v42, v233, v42, vcc
	v_cmp_lt_i32_e32 vcc, v67, v0
	v_add_u32_e32 v67, 18, v66
	s_nop 0
	v_cndmask_b32_e32 v43, v233, v43, vcc
	v_cmp_lt_i32_e32 vcc, v67, v0
	v_add_u32_e32 v67, 19, v66
	s_nop 0
	v_cndmask_b32_e32 v44, v233, v44, vcc
	v_cmp_lt_i32_e32 vcc, v67, v0
	v_add_u32_e32 v67, 24, v66
	s_nop 0
	v_cndmask_b32_e32 v45, v233, v45, vcc
	v_cmp_lt_i32_e32 vcc, v67, v0
	v_add_u32_e32 v67, 25, v66
	s_nop 0
	v_cndmask_b32_e32 v46, v233, v46, vcc
	v_cmp_lt_i32_e32 vcc, v67, v0
	v_add_u32_e32 v67, 26, v66
	s_nop 0
	v_cndmask_b32_e32 v47, v233, v47, vcc
	v_cmp_lt_i32_e32 vcc, v67, v0
	v_add_u32_e32 v67, 27, v66
	s_nop 0
	v_cndmask_b32_e32 v48, v233, v48, vcc
	v_cmp_lt_i32_e32 vcc, v67, v0
	v_add_u32_e32 v67, 32, v66
	s_nop 0
	v_cndmask_b32_e32 v49, v233, v49, vcc
	v_cmp_lt_i32_e32 vcc, v67, v0
	v_add_u32_e32 v67, 33, v66
	s_nop 0
	v_cndmask_b32_e32 v50, v233, v50, vcc
	v_cmp_lt_i32_e32 vcc, v67, v0
	v_add_u32_e32 v67, 34, v66
	s_nop 0
	v_cndmask_b32_e32 v51, v233, v51, vcc
	v_cmp_lt_i32_e32 vcc, v67, v0
	v_add_u32_e32 v67, 35, v66
	s_nop 0
	v_cndmask_b32_e32 v52, v233, v52, vcc
	v_cmp_lt_i32_e32 vcc, v67, v0
	v_add_u32_e32 v67, 40, v66
	s_nop 0
	v_cndmask_b32_e32 v53, v233, v53, vcc
	v_cmp_lt_i32_e32 vcc, v67, v0
	v_add_u32_e32 v67, 41, v66
	s_nop 0
	v_cndmask_b32_e32 v54, v233, v54, vcc
	v_cmp_lt_i32_e32 vcc, v67, v0
	v_add_u32_e32 v67, 42, v66
	s_nop 0
	v_cndmask_b32_e32 v55, v233, v55, vcc
	v_cmp_lt_i32_e32 vcc, v67, v0
	v_add_u32_e32 v67, 43, v66
	s_nop 0
	v_cndmask_b32_e32 v56, v233, v56, vcc
	v_cmp_lt_i32_e32 vcc, v67, v0
	v_add_u32_e32 v67, 48, v66
; template <int MODE, int MK  , bool FIRST, class ValidF> ...
;     ...
;     if (MK != 0) {
; #pragma unroll
;         for (int mt = 0; mt < 2; ++mt)
; #pragma unroll
;             for (int r = 0; r < 16; ++r) { const int kc = 32 * mt + (r & 3) + 8 * (r >> 2); const bool ok = (MK == 2) ? valid(kc + 4 * hh) : lv; p[mt][r] = ok ? p[mt][r] : -INFINITY; } }
;     if (MODE != 1) {
;         float tmax = fmaxf(p[0][0], p[1][0]);
; #pragma unroll
;         for (int r = 1; r < 16; ++r) tmax = fmaxf(tmax, fmaxf(p[0][r], p[1][r]));
;         tmax = fmaxf(tmax, __shfl_xor(tmax, 32));
;         if (MODE == 0) {
;             const float mn = fmaxf(m, tmax); const float mm = (mn == -INFINITY) ? 0.f : mn; l *= __builtin_amdgcn_exp2f(m - mm); m = mn;
; #pragma unroll
;             for (int mt = 0; mt < 2; ++mt)
; #pragma unroll
;                 for (int r = 0; r < 16; ++r) p[mt][r] -= mm;
;         } else if (FIRST) {
;             m = tmax;
; #pragma unroll
;             for (int mt = 0; mt < 2; ++mt)
; #pragma unroll
;                 for (int r = 0; r < 16; ++r) p[mt][r] -= tmax;
;         } else if (__any(tmax > 8.0f)) {
;             const float dl = fmaxf(tmax, 0.f); m += dl; const float f = __builtin_amdgcn_exp2f(-dl); l *= f;
; #pragma unroll
;             for (int mt = 0; mt < 2; ++mt)
; #pragma unroll
;                 for (int r = 0; r < 16; ++r) p[mt][r] -= dl;
; #pragma unroll
;             for (int i = 0; i < 16; ++i) { o[0][i] *= f; o[1][i] *= f; } }
;     }
;     float ls = 0.f;
; #pragma unroll
;     for (int mt = 0; mt < 2; ++mt)
; #pragma unroll
;         for (int r = 0; r < 16; ++r) { const float e = __builtin_amdgcn_exp2f(p[mt][r]); p[mt][r] = e; ls += e; }
;     l += ls;
	s_nop 0
	v_cndmask_b32_e32 v57, v233, v57, vcc
	v_cmp_lt_i32_e32 vcc, v67, v0
	v_add_u32_e32 v67, 49, v66
	s_nop 0
	v_cndmask_b32_e32 v58, v233, v58, vcc
	v_cmp_lt_i32_e32 vcc, v67, v0
	v_add_u32_e32 v67, 50, v66
	s_nop 0
	v_cndmask_b32_e32 v59, v233, v59, vcc
	v_cmp_lt_i32_e32 vcc, v67, v0
	v_add_u32_e32 v67, 51, v66
	s_nop 0
	v_cndmask_b32_e32 v60, v233, v60, vcc
	v_cmp_lt_i32_e32 vcc, v67, v0
	v_add_u32_e32 v67, 56, v66
	s_nop 0
	v_cndmask_b32_e32 v61, v233, v61, vcc
	v_cmp_lt_i32_e32 vcc, v67, v0
	v_add_u32_e32 v67, 57, v66
	s_nop 0
	v_cndmask_b32_e32 v62, v233, v62, vcc
	v_cmp_lt_i32_e32 vcc, v67, v0
	v_add_u32_e32 v67, 58, v66
	v_add_u32_e32 v66, 59, v66
	v_cndmask_b32_e32 v63, v233, v63, vcc
	v_cmp_lt_i32_e32 vcc, v67, v0
	v_max_f32_e32 v67, v36, v36
	s_nop 0
	v_cndmask_b32_e32 v64, v233, v64, vcc
	v_cmp_lt_i32_e32 vcc, v66, v0
	v_max_f32_e32 v66, v35, v35
	s_nop 0
	v_cndmask_b32_e32 v0, v233, v65, vcc
	v_max_f32_e32 v65, v51, v51
	v_max_f32_e32 v65, v66, v65
	v_max_f32_e32 v66, v52, v52
	v_max_f32_e32 v66, v67, v66
	v_max_f32_e32 v67, v53, v53
	v_max3_f32 v65, v34, v50, v65
	v_max_f32_e32 v67, v68, v67
	v_max3_f32 v65, v65, v66, v67
	v_max_f32_e32 v66, v54, v54
	v_max_f32_e32 v67, v38, v38
	v_max_f32_e32 v66, v67, v66
	v_max_f32_e32 v67, v55, v55
	v_max_f32_e32 v68, v39, v39
	v_max_f32_e32 v67, v68, v67
	v_max3_f32 v65, v65, v66, v67
	v_max_f32_e32 v66, v56, v56
	v_max_f32_e32 v67, v40, v40
	v_max_f32_e32 v66, v67, v66
	v_max_f32_e32 v67, v57, v57
	v_max_f32_e32 v68, v41, v41
	v_max_f32_e32 v67, v68, v67
	v_max3_f32 v65, v65, v66, v67
	v_max_f32_e32 v66, v58, v58
	v_max_f32_e32 v67, v42, v42
	v_max_f32_e32 v66, v67, v66
	v_max_f32_e32 v67, v59, v59
	v_max_f32_e32 v68, v43, v43
	v_max_f32_e32 v67, v68, v67
	v_max3_f32 v65, v65, v66, v67
	v_max_f32_e32 v66, v60, v60
	v_max_f32_e32 v67, v44, v44
	v_max_f32_e32 v66, v67, v66
	v_max_f32_e32 v67, v61, v61
	v_max_f32_e32 v68, v45, v45
	v_max_f32_e32 v67, v68, v67
	v_max3_f32 v65, v65, v66, v67
	v_max_f32_e32 v66, v62, v62
	v_max_f32_e32 v67, v46, v46
	v_max_f32_e32 v66, v67, v66
	v_max_f32_e32 v67, v63, v63
	v_max_f32_e32 v68, v47, v47
	v_max_f32_e32 v67, v68, v67
	v_max3_f32 v65, v65, v66, v67
	v_max_f32_e32 v66, v64, v64
	v_max_f32_e32 v67, v48, v48
	v_max_f32_e32 v66, v67, v66
	v_max_f32_e32 v67, v0, v0
	v_max_f32_e32 v68, v49, v49
	v_max_f32_e32 v67, v68, v67
	v_max3_f32 v65, v65, v66, v67
	v_mov_b32_e32 v66, v65
	s_nop 1
	v_permlane32_swap_b32_e32 v65, v66
	s_waitcnt lgkmcnt(0)
	v_max3_f32 v65, v93, v65, v66
	v_cmp_neq_f32_e32 vcc, s17, v65
	s_nop 1
	v_cndmask_b32_e32 v66, 0, v65, vcc
	v_sub_f32_e32 v34, v34, v66
	v_sub_f32_e32 v35, v35, v66
	v_exp_f32_e32 v34, v34
	v_exp_f32_e32 v35, v35
	v_sub_f32_e32 v36, v36, v66
	v_sub_f32_e32 v37, v37, v66
	v_add_f32_e32 v34, 0, v34
	v_add_f32_e32 v34, v35, v34
	v_exp_f32_e32 v35, v36
	v_sub_f32_e32 v38, v38, v66
	v_sub_f32_e32 v39, v39, v66
	v_sub_f32_e32 v40, v40, v66
	v_add_f32_e32 v34, v35, v34
	v_exp_f32_e32 v35, v37
	v_sub_f32_e32 v41, v41, v66
	v_sub_f32_e32 v42, v42, v66
	v_sub_f32_e32 v43, v43, v66
	v_add_f32_e32 v34, v35, v34
	v_exp_f32_e32 v35, v38
	v_sub_f32_e32 v44, v44, v66
	v_sub_f32_e32 v45, v45, v66
	v_sub_f32_e32 v46, v46, v66
	v_add_f32_e32 v34, v35, v34
	v_exp_f32_e32 v35, v39
	v_sub_f32_e32 v47, v47, v66
	v_sub_f32_e32 v48, v48, v66
	v_sub_f32_e32 v49, v49, v66
	v_add_f32_e32 v34, v35, v34
	v_exp_f32_e32 v35, v40
	v_sub_f32_e32 v50, v50, v66
	v_sub_f32_e32 v51, v51, v66
	v_sub_f32_e32 v52, v52, v66
	v_add_f32_e32 v34, v35, v34
	v_exp_f32_e32 v35, v41
	v_sub_f32_e32 v53, v53, v66
	v_sub_f32_e32 v54, v54, v66
	v_sub_f32_e32 v55, v55, v66
	v_add_f32_e32 v34, v35, v34
	v_exp_f32_e32 v35, v42
	v_sub_f32_e32 v56, v56, v66
	v_sub_f32_e32 v57, v57, v66
	v_sub_f32_e32 v58, v58, v66
	v_add_f32_e32 v34, v35, v34
	v_exp_f32_e32 v35, v43
	v_sub_f32_e32 v59, v59, v66
	v_sub_f32_e32 v60, v60, v66
	v_sub_f32_e32 v61, v61, v66
	v_add_f32_e32 v34, v35, v34
	v_exp_f32_e32 v35, v44
	v_sub_f32_e32 v62, v62, v66
	v_sub_f32_e32 v63, v63, v66
	v_sub_f32_e32 v64, v64, v66
	v_add_f32_e32 v34, v35, v34
	v_exp_f32_e32 v35, v45
	v_sub_f32_e32 v0, v0, v66
	v_sub_f32_e32 v67, v93, v66
	v_exp_f32_e32 v0, v0
	v_add_f32_e32 v34, v35, v34
	v_exp_f32_e32 v35, v46
	v_exp_f32_e32 v67, v67
	v_mov_b32_e32 v93, v65
	v_add_f32_e32 v34, v35, v34
	v_exp_f32_e32 v35, v47
	s_nop 0
	v_add_f32_e32 v34, v35, v34
	v_exp_f32_e32 v35, v48
	s_nop 0
	v_add_f32_e32 v34, v35, v34
	v_exp_f32_e32 v35, v49
	s_nop 0
	v_add_f32_e32 v34, v35, v34
	v_exp_f32_e32 v35, v50
	s_nop 0
	v_add_f32_e32 v34, v35, v34
	v_exp_f32_e32 v35, v51
	s_nop 0
	v_add_f32_e32 v34, v35, v34
	v_exp_f32_e32 v35, v52
	s_nop 0
	v_add_f32_e32 v34, v35, v34
	v_exp_f32_e32 v35, v53
	s_nop 0
	v_add_f32_e32 v34, v35, v34
	v_exp_f32_e32 v35, v54
	s_nop 0
	v_add_f32_e32 v34, v35, v34
	v_exp_f32_e32 v35, v55
	s_nop 0
	v_add_f32_e32 v34, v35, v34
	v_exp_f32_e32 v35, v56
	s_nop 0
	v_add_f32_e32 v34, v35, v34
	v_exp_f32_e32 v35, v57
	s_nop 0
	v_add_f32_e32 v34, v35, v34
	v_exp_f32_e32 v35, v58
	s_nop 0
	v_add_f32_e32 v34, v35, v34
	v_exp_f32_e32 v35, v59
	s_nop 0
	v_add_f32_e32 v34, v35, v34
	v_exp_f32_e32 v35, v60
	s_nop 0
	v_add_f32_e32 v34, v35, v34
	v_exp_f32_e32 v35, v61
	s_nop 0
	v_add_f32_e32 v34, v35, v34
	v_exp_f32_e32 v35, v62
	s_nop 0
	v_add_f32_e32 v34, v35, v34
	v_exp_f32_e32 v35, v63
	s_nop 0
	v_add_f32_e32 v34, v35, v34
	v_exp_f32_e32 v35, v64
	s_nop 0
	v_add_f32_e32 v34, v35, v34
	v_add_f32_e32 v0, v0, v34
	v_fmac_f32_e32 v0, v91, v67
	v_mov_b32_e32 v91, v0

; #define NSA_WAIT_BAR(n) asm volatile("s_waitcnt vmcnt(" #n ") lgkmcnt(0)\n\ts_barrier" ::: "memory")
; __device__ __forceinline__ void nsa_mfma_phase(Frame& F, int l, bf16* YC, int ypitch) {
;     ...
;             NSA_WAIT_BAR(0);
;             if (pass == 0) { const float lt = lsum + __shfl_xor(lsum, 32); m = (lt > 0.f) ? m + __log2f(lt) : 0.f; lsum = 0.f; }
.LBB0_499:
	s_waitcnt vmcnt(0) lgkmcnt(0)
	s_barrier
	s_and_b64 vcc, exec, s[60:61]
	s_cbranch_vccz .LBB0_483
	v_mov_b32_e32 v0, v91
	s_nop 1
	v_permlane32_swap_b32_e32 v91, v0
	s_waitcnt lgkmcnt(0)
	v_add_f32_e32 v0, v91, v0
	v_cmp_lt_f32_e32 vcc, 0, v0
	v_log_f32_e32 v0, v0
	v_mov_b32_e32 v91, 0
	v_add_f32_e32 v0, v93, v0
	v_cndmask_b32_e32 v93, 0, v0, vcc
	s_branch .LBB0_483

; #define LAS __attribute__((address_space(3)))
; template <int MODE, int MK  , bool FIRST, class ValidF> ...
;     int ln = L.lane; asm volatile("" : "+v"(ln));
;     const int r32 = ln & 31, hh = ln >> 5;
;     unsigned kofs[4], vofs[2];
; #pragma unroll
;     for (int ks = 0; ks < 4; ++ks) kofs[ks] = (unsigned)(r32 * 128 + (((2 * ks + hh) ^ (r32 & 7)) << 4));
;     { const int q4 = (ln & 15) >> 2, p4 = ln & 3, blk = (ln >> 4) & 1, cc0 = 2 * blk + (p4 >> 1), kk = 4 * hh + q4;
; #pragma unroll
;         for (int dt = 0; dt < 2; ++dt) vofs[dt] = (unsigned)((4 * hh + q4) * 128 + (((cc0 + 4 * dt) ^ kk) << 4) + 8 * (p4 & 1)); }
;     f32x16 p[2];
;     const float cref = c0 + sbk * (float)(4 * hh) - ((MODE == 2 && !FIRST) || MODE == 1 ? m : 0.f);
; #pragma unroll
;     for (int mt = 0; mt < 2; ++mt)
; #pragma unroll
;         for (int r = 0; r < 16; ++r) p[mt][r] = fmaf(sbk, (float)(32 * mt + (r & 3) + 8 * (r >> 2)), cref);
; #pragma unroll
;     for (int ks = 0; ks < 4; ++ks)
; #pragma unroll
;         for (int mt = 0; mt < 2; ++mt) { const bf16x8 a = *(const LAS bf16x8*)(Kb + kofs[ks] + mt * 4096); p[mt] = MFMA32(a, qf[ks], p[mt]); }
;     if (MK != 0) {
; #pragma unroll
;         for (int mt = 0; mt < 2; ++mt)
; #pragma unroll
;             for (int r = 0; r < 16; ++r) { const int kc = 32 * mt + (r & 3) + 8 * (r >> 2); const bool ok = (MK == 2) ? valid(kc + 4 * hh) : lv; p[mt][r] = ok ? p[mt][r] : -INFINITY; } }
; __device__ __forceinline__ void nsa_mfma_phase(Frame& F, int l, bf16* YC, int ypitch) {
;     ...
;                 if (live && j != c) { const bool selj0 = (mym >> j) & 1ull;
;                     const float bound = ((LAS float*)(lds + L_QN))[w * 64 + lane] * ((LAS float*)(lds + L_KMX))[j] + slope2 * (float)(64 * (j - c) + 63) - m; live = !__all(!selj0 || bound < -40.0f); }
;                 if (live) {
;                     const bool selj = (mym >> j) & 1ull; const bool diag = (j == c); int tq = L.tq; asm volatile("" : "+v"(tq));
;                     auto valid = [&](int koff) { return selj && (!diag || koff <= tq); };
;                     const LAS unsigned char* Kb = lds + L_K + slot * TB; const LAS unsigned char* Vb = lds + L_V + slot * TB;
;                     if (diag) tile_compute<2, 2, true>(Kb, Vb, qf, slope2 * (float)(64 * (j - c)), slope2, selj, valid, m, lsum, o, IMP, L);
.LBB0_526:
	s_andn2_b64 vcc, exec, s[10:11]
	s_cbranch_vccnz .LBB0_540
	s_lshl_b32 s0, s12, 13
	s_waitcnt lgkmcnt(0)
	v_lshrrev_b64 v[82:83], s8, v[34:35]
	v_mov_b32_e32 v66, v124
	s_add_i32 s10, s0, 0
	s_andn2_b64 vcc, exec, s[2:3]
	s_mov_b64 s[0:1], -1
	s_cbranch_vccnz .LBB0_529
	v_mov_b32_e32 v67, v123
	v_mov_b32_e32 v117, v116
	v_ashrrev_i32_e32 v0, 5, v67
	v_lshlrev_b32_e32 v34, 7, v67
	v_and_b32_e32 v72, 0xf80, v34
	v_bitop3_b32 v34, v0, v67, 7 bitop3:0x78
	v_lshlrev_b32_e32 v50, 4, v34
	v_add_u32_e32 v34, 2, v0
	v_add3_u32 v54, s10, v50, v72
	v_bitop3_b32 v34, v34, v67, 7 bitop3:0x78
	ds_read_b128 v[50:53], v54
	ds_read_b128 v[68:71], v54 offset:4096
	v_lshlrev_b32_e32 v73, 4, v34
	v_add_u32_e32 v34, 4, v0
	v_bitop3_b32 v34, v34, v67, 7 bitop3:0x78
	v_lshlrev_b32_e32 v76, 2, v0
	v_lshlrev_b32_e32 v74, 4, v34
	v_add_u32_e32 v34, 6, v0
	v_cvt_f32_i32_e32 v0, v76
	v_bitop3_b32 v34, v34, v67, 7 bitop3:0x78
	v_lshlrev_b32_e32 v75, 4, v34
	v_cmp_le_i32_e64 s[0:1], v76, v66
	v_fma_f32 v0, v116, v0, v129
	v_fma_f32 v34, 0, v116, v0
	v_add_f32_e32 v35, v116, v0
	v_pk_fma_f32 v[36:37], v[118:119], s[18:19], v[0:1] op_sel_hi:[1,1,0]
	v_pk_fma_f32 v[38:39], v[118:119], s[74:75], v[0:1] op_sel_hi:[1,1,0]
	v_pk_fma_f32 v[40:41], v[118:119], s[36:37], v[0:1] op_sel_hi:[1,1,0]
	v_pk_fma_f32 v[42:43], v[118:119], s[26:27], v[0:1] op_sel_hi:[1,1,0]
	v_pk_fma_f32 v[44:45], v[118:119], s[56:57], v[0:1] op_sel_hi:[1,1,0]
	v_pk_fma_f32 v[46:47], v[118:119], s[22:23], v[0:1] op_sel_hi:[1,1,0]
	v_pk_fma_f32 v[48:49], v[118:119], s[24:25], v[0:1] op_sel_hi:[1,1,0]
	v_pk_fma_f32 v[64:65], v[116:117], s[30:31], v[0:1] op_sel_hi:[1,1,0]
	v_pk_fma_f32 v[62:63], v[116:117], s[20:21], v[0:1] op_sel_hi:[1,1,0]
	s_waitcnt lgkmcnt(1)
	v_mfma_f32_32x32x16_bf16 v[34:49], v[50:53], v[98:101], v[34:49]
	v_fma_f32 v60, v116, s34, v0
	v_fma_f32 v61, v117, s35, v0
	v_fma_f32 v58, v116, s80, v0
	v_fma_f32 v59, v117, s81, v0
	v_fma_f32 v56, v116, s76, v0
	v_fma_f32 v57, v117, s77, v0
	v_pk_fma_f32 v[54:55], v[116:117], s[82:83], v[0:1] op_sel_hi:[1,1,0]
	v_pk_fma_f32 v[52:53], v[116:117], s[84:85], v[0:1] op_sel_hi:[1,1,0]
	v_pk_fma_f32 v[50:51], v[120:121], s[86:87], v[0:1] op_sel_hi:[1,1,0]
	v_add3_u32 v0, s10, v73, v72
	s_waitcnt lgkmcnt(0)
	v_mfma_f32_32x32x16_bf16 v[50:65], v[68:71], v[98:101], v[50:65]
	ds_read_b128 v[68:71], v0
	s_waitcnt lgkmcnt(0)
	v_mfma_f32_32x32x16_bf16 v[34:49], v[68:71], v[102:105], v[34:49]
	ds_read_b128 v[68:71], v0 offset:4096
	v_add3_u32 v0, s10, v74, v72
	s_waitcnt lgkmcnt(0)
	v_mfma_f32_32x32x16_bf16 v[50:65], v[68:71], v[102:105], v[50:65]
	ds_read_b128 v[68:71], v0
	s_waitcnt lgkmcnt(0)
	v_mfma_f32_32x32x16_bf16 v[34:49], v[68:71], v[106:109], v[34:49]
	ds_read_b128 v[68:71], v0 offset:4096
	v_add3_u32 v0, s10, v75, v72
	s_waitcnt lgkmcnt(0)
	v_mfma_f32_32x32x16_bf16 v[50:65], v[68:71], v[106:109], v[50:65]
	ds_read_b128 v[68:71], v0
	s_waitcnt lgkmcnt(0)
	v_mfma_f32_32x32x16_bf16 v[34:49], v[68:71], v[110:113], v[34:49]
	ds_read_b128 v[68:71], v0 offset:4096
	v_and_b32_e32 v0, 1, v82
	v_cmp_eq_u32_e32 vcc, 1, v0
	s_and_b64 s[0:1], vcc, s[0:1]
	v_or_b32_e32 v0, 2, v76
	s_nop 6
	v_cndmask_b32_e64 v34, v233, v34, s[0:1]
	v_cmp_lt_i32_e64 s[0:1], v76, v66
	s_and_b64 s[0:1], vcc, s[0:1]
	s_waitcnt lgkmcnt(0)
	v_mfma_f32_32x32x16_bf16 v[50:65], v[68:71], v[110:113], v[50:65]
	v_cndmask_b32_e64 v35, v233, v35, s[0:1]
	v_cmp_le_i32_e64 s[0:1], v0, v66
	s_and_b64 s[0:1], vcc, s[0:1]
	v_or_b32_e32 v0, 3, v76
	v_cndmask_b32_e64 v36, v233, v36, s[0:1]
	v_cmp_le_i32_e64 s[0:1], v0, v66
	s_and_b64 s[0:1], vcc, s[0:1]
	v_add_u32_e32 v0, 8, v76
	v_cndmask_b32_e64 v37, v233, v37, s[0:1]
	v_cmp_le_i32_e64 s[0:1], v0, v66
	s_and_b64 s[0:1], vcc, s[0:1]
	v_add_u32_e32 v0, 9, v76
	v_cndmask_b32_e64 v38, v233, v38, s[0:1]
	v_cmp_le_i32_e64 s[0:1], v0, v66
	s_and_b64 s[0:1], vcc, s[0:1]
	v_add_u32_e32 v0, 10, v76
	v_cndmask_b32_e64 v39, v233, v39, s[0:1]
	v_cmp_le_i32_e64 s[0:1], v0, v66
	s_and_b64 s[0:1], vcc, s[0:1]
	v_add_u32_e32 v0, 11, v76
	v_cndmask_b32_e64 v40, v233, v40, s[0:1]
	v_cmp_le_i32_e64 s[0:1], v0, v66
	s_and_b64 s[0:1], vcc, s[0:1]
	v_add_u32_e32 v0, 16, v76
	v_cndmask_b32_e64 v41, v233, v41, s[0:1]
	v_cmp_le_i32_e64 s[0:1], v0, v66
	s_and_b64 s[0:1], vcc, s[0:1]
	v_add_u32_e32 v0, 17, v76
	v_cndmask_b32_e64 v42, v233, v42, s[0:1]
	v_cmp_le_i32_e64 s[0:1], v0, v66
	s_and_b64 s[0:1], vcc, s[0:1]
	v_add_u32_e32 v0, 18, v76
	v_cndmask_b32_e64 v43, v233, v43, s[0:1]
	v_cmp_le_i32_e64 s[0:1], v0, v66
	s_and_b64 s[0:1], vcc, s[0:1]
	v_add_u32_e32 v0, 19, v76
	v_cndmask_b32_e64 v44, v233, v44, s[0:1]
	v_cmp_le_i32_e64 s[0:1], v0, v66
	s_and_b64 s[0:1], vcc, s[0:1]
	v_add_u32_e32 v0, 24, v76
	v_cndmask_b32_e64 v45, v233, v45, s[0:1]
	v_cmp_le_i32_e64 s[0:1], v0, v66
	s_and_b64 s[0:1], vcc, s[0:1]
	v_add_u32_e32 v0, 25, v76
	v_cndmask_b32_e64 v46, v233, v46, s[0:1]
	v_cmp_le_i32_e64 s[0:1], v0, v66
	s_and_b64 s[0:1], vcc, s[0:1]
	v_add_u32_e32 v0, 26, v76
	v_cndmask_b32_e64 v47, v233, v47, s[0:1]
	v_cmp_le_i32_e64 s[0:1], v0, v66
	s_and_b64 s[0:1], vcc, s[0:1]
	v_add_u32_e32 v0, 27, v76
	v_cndmask_b32_e64 v48, v233, v48, s[0:1]
	v_cmp_le_i32_e64 s[0:1], v0, v66
	s_and_b64 s[0:1], vcc, s[0:1]
	v_add_u32_e32 v0, 32, v76
	v_cndmask_b32_e64 v49, v233, v49, s[0:1]
	v_cmp_le_i32_e64 s[0:1], v0, v66
	s_and_b64 s[0:1], vcc, s[0:1]
	s_nop 0
	v_cndmask_b32_e64 v68, v233, v50, s[0:1]
	v_cmp_lt_i32_e64 s[0:1], v0, v66
	s_and_b64 s[0:1], vcc, s[0:1]
	v_add_u32_e32 v0, 34, v76
	v_cndmask_b32_e64 v69, v233, v51, s[0:1]
	v_cmp_le_i32_e64 s[0:1], v0, v66
	s_and_b64 s[0:1], vcc, s[0:1]
	v_add_u32_e32 v0, 35, v76
	v_cndmask_b32_e64 v52, v233, v52, s[0:1]
; template <int MODE, int MK  , bool FIRST, class ValidF> ...
;     ...
;     if (MK != 0) {
; #pragma unroll
;         for (int mt = 0; mt < 2; ++mt)
; #pragma unroll
;             for (int r = 0; r < 16; ++r) { const int kc = 32 * mt + (r & 3) + 8 * (r >> 2); const bool ok = (MK == 2) ? valid(kc + 4 * hh) : lv; p[mt][r] = ok ? p[mt][r] : -INFINITY; } }
;     if (MODE != 1) {
;         float tmax = fmaxf(p[0][0], p[1][0]);
; #pragma unroll
;         for (int r = 1; r < 16; ++r) tmax = fmaxf(tmax, fmaxf(p[0][r], p[1][r]));
;         tmax = fmaxf(tmax, __shfl_xor(tmax, 32));
;         if (MODE == 0) {
;             const float mn = fmaxf(m, tmax); const float mm = (mn == -INFINITY) ? 0.f : mn; l *= __builtin_amdgcn_exp2f(m - mm); m = mn;
; #pragma unroll
;             for (int mt = 0; mt < 2; ++mt)
; #pragma unroll
;                 for (int r = 0; r < 16; ++r) p[mt][r] -= mm;
;         } else if (FIRST) {
;             m = tmax;
; #pragma unroll
;             for (int mt = 0; mt < 2; ++mt)
; #pragma unroll
;                 for (int r = 0; r < 16; ++r) p[mt][r] -= tmax;
;         } else if (__any(tmax > 8.0f)) {
;             const float dl = fmaxf(tmax, 0.f); m += dl; const float f = __builtin_amdgcn_exp2f(-dl); l *= f;
; #pragma unroll
;             for (int mt = 0; mt < 2; ++mt)
; #pragma unroll
;                 for (int r = 0; r < 16; ++r) p[mt][r] -= dl;
; #pragma unroll
;             for (int i = 0; i < 16; ++i) { o[0][i] *= f; o[1][i] *= f; } }
;     }
;     float ls = 0.f;
; #pragma unroll
;     for (int mt = 0; mt < 2; ++mt)
; #pragma unroll
;         for (int r = 0; r < 16; ++r) { const float e = __builtin_amdgcn_exp2f(p[mt][r]); p[mt][r] = e; ls += e; }
;     l += ls;
;     if (MODE == 0) return;
;     if (MODE == 1) {
;         float av[8], bv[8];
; #pragma unroll
;         for (int mt = 0; mt < 2; ++mt)
; #pragma unroll
;             for (int g4 = 0; g4 < 4; ++g4) { const float h3 = 0.5f * p[mt][4 * g4 + 3]; av[mt * 4 + g4] = (p[mt][4 * g4] + p[mt][4 * g4 + 1]) + (p[mt][4 * g4 + 2] + h3); bv[mt * 4 + g4] = h3; }
; #pragma unroll
;         for (int i = 0; i < 8; ++i) imp[8 * (i >> 2) + 2 * (i & 3) + hh] += av[i];
;         asm volatile("s_waitcnt lgkmcnt(0)" ::: "memory"); __builtin_amdgcn_wave_barrier();
; #pragma unroll
;         for (int i = 0; i < 8; ++i) imp[8 * (i >> 2) + 2 * (i & 3) + hh + 1] += bv[i];
	v_cmp_le_i32_e64 s[0:1], v0, v66
	s_and_b64 s[0:1], vcc, s[0:1]
	v_add_u32_e32 v0, 40, v76
	v_cndmask_b32_e64 v53, v233, v53, s[0:1]
	v_cmp_le_i32_e64 s[0:1], v0, v66
	s_and_b64 s[0:1], vcc, s[0:1]
	v_add_u32_e32 v0, 41, v76
	v_cndmask_b32_e64 v54, v233, v54, s[0:1]
	v_cmp_le_i32_e64 s[0:1], v0, v66
	s_and_b64 s[0:1], vcc, s[0:1]
	v_add_u32_e32 v0, 42, v76
	v_cndmask_b32_e64 v55, v233, v55, s[0:1]
	v_cmp_le_i32_e64 s[0:1], v0, v66
	s_and_b64 s[0:1], vcc, s[0:1]
	v_add_u32_e32 v0, 43, v76
	v_cndmask_b32_e64 v56, v233, v56, s[0:1]
	v_cmp_le_i32_e64 s[0:1], v0, v66
	s_and_b64 s[0:1], vcc, s[0:1]
	v_add_u32_e32 v0, 48, v76
	v_cndmask_b32_e64 v57, v233, v57, s[0:1]
	v_cmp_le_i32_e64 s[0:1], v0, v66
	s_and_b64 s[0:1], vcc, s[0:1]
	v_add_u32_e32 v0, 49, v76
	v_cndmask_b32_e64 v58, v233, v58, s[0:1]
	v_cmp_le_i32_e64 s[0:1], v0, v66
	s_and_b64 s[0:1], vcc, s[0:1]
	v_add_u32_e32 v0, 50, v76
	v_cndmask_b32_e64 v59, v233, v59, s[0:1]
	v_cmp_le_i32_e64 s[0:1], v0, v66
	s_and_b64 s[0:1], vcc, s[0:1]
	v_add_u32_e32 v0, 51, v76
	v_cndmask_b32_e64 v60, v233, v60, s[0:1]
	v_cmp_le_i32_e64 s[0:1], v0, v66
	s_and_b64 s[0:1], vcc, s[0:1]
	v_add_u32_e32 v0, 56, v76
	v_cndmask_b32_e64 v61, v233, v61, s[0:1]
	v_cmp_le_i32_e64 s[0:1], v0, v66
	s_and_b64 s[0:1], vcc, s[0:1]
	v_add_u32_e32 v0, 57, v76
	v_cndmask_b32_e64 v62, v233, v62, s[0:1]
	v_cmp_le_i32_e64 s[0:1], v0, v66
	s_and_b64 s[0:1], vcc, s[0:1]
	v_add_u32_e32 v0, 58, v76
	v_cndmask_b32_e64 v63, v233, v63, s[0:1]
	v_cmp_le_i32_e64 s[0:1], v0, v66
	s_and_b64 s[0:1], vcc, s[0:1]
	v_add_u32_e32 v0, 59, v76
	v_cndmask_b32_e64 v64, v233, v64, s[0:1]
	v_cmp_le_i32_e64 s[0:1], v0, v66
	v_lshrrev_b32_e32 v0, 3, v67
	v_lshrrev_b32_e32 v51, 2, v67
	v_and_b32_e32 v0, 2, v0
	v_bfe_u32 v66, v67, 1, 1
	v_and_or_b32 v70, v51, 3, v76
	v_or_b32_e32 v50, v0, v66
	v_bitop3_b32 v0, v0, v70, v66 bitop3:0x36
	v_lshlrev_b32_e32 v51, 3, v67
	v_lshlrev_b32_e32 v86, 4, v0
	v_max_f32_e32 v0, v69, v69
	v_max_f32_e32 v66, v35, v35
	v_and_b32_e32 v51, 8, v51
	v_max_f32_e32 v0, v66, v0
	v_max_f32_e32 v66, v52, v52
	v_max_f32_e32 v67, v36, v36
	v_bitop3_b32 v50, v50, v70, 4 bitop3:0x36
	v_lshl_or_b32 v51, v70, 7, v51
	v_max_f32_e32 v66, v67, v66
	v_max_f32_e32 v67, v53, v53
	v_max_f32_e32 v70, v37, v37
	v_max3_f32 v0, v34, v68, v0
	v_max_f32_e32 v67, v70, v67
	v_max3_f32 v0, v0, v66, v67
	v_max_f32_e32 v66, v54, v54
	v_max_f32_e32 v67, v38, v38
	v_max_f32_e32 v66, v67, v66
	v_max_f32_e32 v67, v55, v55
	v_max_f32_e32 v70, v39, v39
	v_max_f32_e32 v67, v70, v67
	v_max3_f32 v0, v0, v66, v67
	v_max_f32_e32 v66, v56, v56
	v_max_f32_e32 v67, v40, v40
	v_max_f32_e32 v66, v67, v66
	v_max_f32_e32 v67, v57, v57
	v_max_f32_e32 v70, v41, v41
	v_max_f32_e32 v67, v70, v67
	v_max3_f32 v0, v0, v66, v67
	v_max_f32_e32 v66, v58, v58
	v_max_f32_e32 v67, v42, v42
	v_max_f32_e32 v66, v67, v66
	v_max_f32_e32 v67, v59, v59
	v_max_f32_e32 v70, v43, v43
	v_max_f32_e32 v67, v70, v67
	v_max3_f32 v0, v0, v66, v67
	v_max_f32_e32 v66, v60, v60
	v_max_f32_e32 v67, v44, v44
	v_max_f32_e32 v66, v67, v66
	v_max_f32_e32 v67, v61, v61
	v_max_f32_e32 v70, v45, v45
	v_max_f32_e32 v67, v70, v67
	v_max3_f32 v0, v0, v66, v67
	v_max_f32_e32 v66, v62, v62
	v_max_f32_e32 v67, v46, v46
	v_max_f32_e32 v66, v67, v66
	v_max_f32_e32 v67, v63, v63
	v_max_f32_e32 v70, v47, v47
	s_and_b64 vcc, vcc, s[0:1]
	v_max_f32_e32 v67, v70, v67
	v_cndmask_b32_e32 v65, v233, v65, vcc
	v_max3_f32 v0, v0, v66, v67
	v_max_f32_e32 v66, v64, v64
	v_max_f32_e32 v67, v48, v48
	v_max_f32_e32 v66, v67, v66
	v_max_f32_e32 v67, v65, v65
	v_max_f32_e32 v70, v49, v49
	v_max_f32_e32 v67, v70, v67
	v_max3_f32 v0, v0, v66, v67
	v_mov_b32_e32 v66, v0
	s_nop 1
	v_permlane32_swap_b32_e32 v0, v66
	v_lshlrev_b32_e32 v50, 4, v50
	v_add3_u32 v90, s10, v50, v51
	s_mov_b64 s[0:1], 0
	s_waitcnt lgkmcnt(0)
	v_max_f32_e32 v66, v66, v66
	v_max_f32_e32 v0, v0, v66
	v_sub_f32_e32 v34, v34, v0
	v_sub_f32_e32 v35, v35, v0
	v_exp_f32_e32 v34, v34
	v_sub_f32_e32 v36, v36, v0
	v_exp_f32_e32 v35, v35
	v_sub_f32_e32 v37, v37, v0
	v_exp_f32_e32 v36, v36
	v_sub_f32_e32 v38, v38, v0
	v_exp_f32_e32 v37, v37
	v_sub_f32_e32 v39, v39, v0
	v_sub_f32_e32 v66, v68, v0
	v_add_f32_e32 v68, 0, v34
	v_exp_f32_e32 v38, v38
	v_sub_f32_e32 v40, v40, v0
	v_add_f32_e32 v68, v35, v68
	v_exp_f32_e32 v39, v39
	v_sub_f32_e32 v41, v41, v0
	v_add_f32_e32 v68, v36, v68
	v_exp_f32_e32 v40, v40
	v_sub_f32_e32 v42, v42, v0
	v_add_f32_e32 v68, v37, v68
	v_exp_f32_e32 v41, v41
	v_sub_f32_e32 v43, v43, v0
	v_add_f32_e32 v68, v38, v68
	v_exp_f32_e32 v42, v42
	v_sub_f32_e32 v44, v44, v0
	v_add_f32_e32 v68, v39, v68
	v_exp_f32_e32 v43, v43
	v_sub_f32_e32 v45, v45, v0
	v_add_f32_e32 v68, v40, v68
	v_exp_f32_e32 v44, v44
	v_sub_f32_e32 v46, v46, v0
	v_add_f32_e32 v68, v41, v68
	v_exp_f32_e32 v45, v45
	v_sub_f32_e32 v47, v47, v0
	v_add_f32_e32 v68, v42, v68
	v_exp_f32_e32 v46, v46
	v_sub_f32_e32 v48, v48, v0
	v_add_f32_e32 v68, v43, v68
	v_exp_f32_e32 v47, v47
	v_sub_f32_e32 v49, v49, v0
	v_add_f32_e32 v68, v44, v68
	v_exp_f32_e32 v48, v48
	v_add_f32_e32 v68, v45, v68
	v_exp_f32_e32 v49, v49
	v_sub_f32_e32 v67, v69, v0
	v_add_f32_e32 v68, v46, v68
	v_exp_f32_e32 v66, v66
	v_sub_f32_e32 v52, v52, v0
	v_add_f32_e32 v68, v47, v68
	v_exp_f32_e32 v67, v67
	v_sub_f32_e32 v53, v53, v0
	v_add_f32_e32 v68, v48, v68
	v_exp_f32_e32 v52, v52
	v_sub_f32_e32 v54, v54, v0
	v_add_f32_e32 v68, v49, v68
	v_exp_f32_e32 v53, v53
	v_sub_f32_e32 v55, v55, v0
	v_add_f32_e32 v68, v66, v68
	v_exp_f32_e32 v54, v54
	v_sub_f32_e32 v56, v56, v0
	v_sub_f32_e32 v57, v57, v0
	v_add_f32_e32 v68, v67, v68
	v_exp_f32_e32 v55, v55
	v_add_f32_e32 v68, v52, v68
	v_exp_f32_e32 v56, v56
	v_exp_f32_e32 v57, v57
	v_add_f32_e32 v68, v53, v68
	v_add_f32_e32 v68, v54, v68
	v_add_f32_e32 v68, v55, v68
	v_add_f32_e32 v68, v56, v68
	v_cvt_pk_bf16_f32 v73, v56, v57
	v_add3_u32 v56, s10, v86, v51
	v_cvt_pk_bf16_f32 v71, v52, v53
	v_cvt_pk_bf16_f32 v72, v54, v55
	ds_read_b64_tr_b16 v[52:53], v56 offset:24576
	ds_read_b64_tr_b16 v[54:55], v56 offset:25600
	v_cvt_pk_bf16_f32 v78, v34, v35
	v_cvt_pk_bf16_f32 v79, v36, v37
	v_cvt_pk_bf16_f32 v80, v38, v39
	v_cvt_pk_bf16_f32 v81, v40, v41
	v_cvt_pk_bf16_f32 v74, v42, v43
	v_cvt_pk_bf16_f32 v75, v44, v45
	v_cvt_pk_bf16_f32 v76, v46, v47
	v_cvt_pk_bf16_f32 v77, v48, v49
	v_mov_b64_e32 v[48:49], v[16:17]
	v_mov_b64_e32 v[46:47], v[14:15]
	v_mov_b64_e32 v[44:45], v[12:13]
	v_mov_b64_e32 v[42:43], v[10:11]
	v_mov_b64_e32 v[40:41], v[8:9]
	v_mov_b64_e32 v[38:39], v[6:7]
	v_mov_b64_e32 v[36:37], v[4:5]
	v_mov_b64_e32 v[34:35], v[2:3]
	v_sub_f32_e32 v58, v58, v0
	v_sub_f32_e32 v59, v59, v0
	s_waitcnt lgkmcnt(0)
; #define LAS __attribute__((address_space(3)))
; __device__ __forceinline__ s16x4 vtr(const LAS unsigned char* p) { typedef short v4 __attribute__((ext_vector_type(4))); return __builtin_bit_cast(s16x4, __builtin_amdgcn_ds_read_tr16_b64_v4i16((LAS v4*)p)); }
; #define MFMA32(a, b, c) __builtin_amdgcn_mfma_f32_32x32x16_bf16((a), (b), (c), 0, 0, 0)
; template <int MODE, int MK  , bool FIRST, class ValidF> ...
;     ...
;     const float cref = c0 + sbk * (float)(4 * hh) - ((MODE == 2 && !FIRST) || MODE == 1 ? m : 0.f);
; #pragma unroll
;     for (int mt = 0; mt < 2; ++mt)
; #pragma unroll
;         for (int r = 0; r < 16; ++r) p[mt][r] = fmaf(sbk, (float)(32 * mt + (r & 3) + 8 * (r >> 2)), cref);
; #pragma unroll
;     for (int ks = 0; ks < 4; ++ks)
; #pragma unroll
;         for (int mt = 0; mt < 2; ++mt) { const bf16x8 a = *(const LAS bf16x8*)(Kb + kofs[ks] + mt * 4096); p[mt] = MFMA32(a, qf[ks], p[mt]); }
;     ...
; #pragma unroll
;     for (int dt = 0; dt < 2; ++dt)
; #pragma unroll
;         for (int mt = 0; mt < 2; ++mt)
; #pragma unroll
;             for (int sg = 0; sg < 2; ++sg) { const LAS unsigned char* vp = Vb + vofs[dt] + (32 * mt + 16 * sg) * 128;
;                 const s16x4 lo = vtr(vp), hi = vtr(vp + 8 * 128); const bf16x8 vf = __builtin_shufflevector(lo, hi, 0, 1, 2, 3, 4, 5, 6, 7);
;                 o[dt] = MFMA32(vf, pf[mt][sg], o[dt]); }
	v_mfma_f32_32x32x16_bf16 v[34:49], v[52:55], v[78:81], v[34:49]
	ds_read_b64_tr_b16 v[52:53], v56 offset:26624
	ds_read_b64_tr_b16 v[54:55], v56 offset:27648
	v_exp_f32_e32 v58, v58
	v_sub_f32_e32 v60, v60, v0
	v_exp_f32_e32 v59, v59
	v_sub_f32_e32 v61, v61, v0
	v_exp_f32_e32 v60, v60
	v_sub_f32_e32 v62, v62, v0
	s_waitcnt lgkmcnt(0)
	v_mfma_f32_32x32x16_bf16 v[34:49], v[52:55], v[74:77], v[34:49]
	ds_read_b64_tr_b16 v[52:53], v56 offset:28672
	ds_read_b64_tr_b16 v[54:55], v56 offset:29696
	v_add_f32_e32 v68, v57, v68
	v_exp_f32_e32 v61, v61
	v_sub_f32_e32 v63, v63, v0
	v_add_f32_e32 v68, v58, v68
	v_exp_f32_e32 v62, v62
	v_cvt_pk_bf16_f32 v70, v66, v67
	v_sub_f32_e32 v64, v64, v0
	v_add_f32_e32 v68, v59, v68
	v_exp_f32_e32 v63, v63
	s_waitcnt lgkmcnt(0)
	v_mfma_f32_32x32x16_bf16 v[34:49], v[52:55], v[70:73], v[34:49]
	v_sub_f32_e32 v65, v65, v0
	v_add_f32_e32 v68, v60, v68
	v_exp_f32_e32 v64, v64
	v_add_f32_e32 v68, v61, v68
	v_exp_f32_e32 v65, v65
	v_add_f32_e32 v68, v62, v68
	ds_read_b64_tr_b16 v[52:53], v56 offset:30720
	ds_read_b64_tr_b16 v[54:55], v56 offset:31744
	v_add_f32_e32 v68, v63, v68
	v_add_f32_e32 v68, v64, v68
	ds_read_b64_tr_b16 v[86:87], v90 offset:24576
	ds_read_b64_tr_b16 v[88:89], v90 offset:25600
	v_add_f32_e32 v68, v65, v68
	v_add_f32_e32 v83, v85, v68
	v_cvt_pk_bf16_f32 v66, v58, v59
	v_cvt_pk_bf16_f32 v67, v60, v61
	v_cvt_pk_bf16_f32 v68, v62, v63
	v_cvt_pk_bf16_f32 v69, v64, v65
	s_waitcnt lgkmcnt(2)
	s_nop 0
	v_mfma_f32_32x32x16_bf16 v[34:49], v[52:55], v[66:69], v[34:49]
	v_mov_b64_e32 v[64:65], v[32:33]
	v_mov_b64_e32 v[62:63], v[30:31]
	v_mov_b64_e32 v[60:61], v[28:29]
	v_mov_b64_e32 v[58:59], v[26:27]
	v_mov_b64_e32 v[56:57], v[24:25]
	v_mov_b64_e32 v[54:55], v[22:23]
	v_mov_b64_e32 v[52:53], v[20:21]
	v_mov_b64_e32 v[50:51], v[18:19]
	s_waitcnt lgkmcnt(0)
	s_nop 0
	v_mfma_f32_32x32x16_bf16 v[50:65], v[86:89], v[78:81], v[50:65]
	ds_read_b64_tr_b16 v[78:79], v90 offset:26624
	ds_read_b64_tr_b16 v[80:81], v90 offset:27648
	s_waitcnt lgkmcnt(0)
	v_mfma_f32_32x32x16_bf16 v[50:65], v[78:81], v[74:77], v[50:65]
	ds_read_b64_tr_b16 v[74:75], v90 offset:28672
	ds_read_b64_tr_b16 v[76:77], v90 offset:29696
	s_waitcnt lgkmcnt(0)
	v_mfma_f32_32x32x16_bf16 v[50:65], v[74:77], v[70:73], v[50:65]
	ds_read_b64_tr_b16 v[70:71], v90 offset:30720
	ds_read_b64_tr_b16 v[72:73], v90 offset:31744
	s_waitcnt lgkmcnt(0)
	v_mfma_f32_32x32x16_bf16 v[50:65], v[70:73], v[66:69], v[50:65]
.LBB0_529:
	s_andn2_b64 vcc, exec, s[0:1]
	s_cbranch_vccnz .LBB0_539
	s_sub_i32 s0, s8, s70
	s_lshl_b32 s0, s0, 6
	v_cvt_f32_i32_e32 v0, s0
	v_and_b32_e32 v66, 1, v82
	v_cmp_ne_u32_e32 vcc, 0, v66
	s_cmp_lg_u64 vcc, exec
	v_mul_f32_e32 v82, v116, v0
	s_mov_b64 s[0:1], -1
	s_cbranch_scc0 .LBB0_535
	v_cmp_eq_u32_e32 vcc, 1, v66
	v_mov_b32_e32 v66, v123
	v_mov_b32_e32 v117, v116
	v_ashrrev_i32_e32 v0, 5, v66
	v_lshlrev_b32_e32 v34, 7, v66
	v_and_b32_e32 v72, 0xf80, v34
	v_bitop3_b32 v34, v0, v66, 7 bitop3:0x78
	v_lshlrev_b32_e32 v50, 4, v34
	v_add_u32_e32 v34, 2, v0
	v_bitop3_b32 v34, v34, v66, 7 bitop3:0x78
	v_add3_u32 v54, s10, v50, v72
	v_lshlrev_b32_e32 v73, 4, v34
	v_add_u32_e32 v34, 4, v0
	ds_read_b128 v[50:53], v54
	ds_read_b128 v[68:71], v54 offset:4096
	v_bitop3_b32 v34, v34, v66, 7 bitop3:0x78
	v_lshlrev_b32_e32 v67, 2, v0
	v_lshlrev_b32_e32 v74, 4, v34
	v_add_u32_e32 v34, 6, v0
	v_cvt_f32_i32_e32 v0, v67
	v_bitop3_b32 v34, v34, v66, 7 bitop3:0x78
	v_lshlrev_b32_e32 v75, 4, v34
	v_fma_f32 v0, v116, v0, v82
	v_sub_f32_e32 v0, v0, v84
	v_fma_f32 v34, 0, v116, v0
	v_add_f32_e32 v35, v116, v0
	v_pk_fma_f32 v[36:37], v[118:119], s[18:19], v[0:1] op_sel_hi:[1,1,0]
	v_pk_fma_f32 v[38:39], v[118:119], s[74:75], v[0:1] op_sel_hi:[1,1,0]
	v_pk_fma_f32 v[40:41], v[118:119], s[36:37], v[0:1] op_sel_hi:[1,1,0]
	v_pk_fma_f32 v[42:43], v[118:119], s[26:27], v[0:1] op_sel_hi:[1,1,0]
	v_pk_fma_f32 v[44:45], v[118:119], s[56:57], v[0:1] op_sel_hi:[1,1,0]
	v_pk_fma_f32 v[46:47], v[118:119], s[22:23], v[0:1] op_sel_hi:[1,1,0]
	v_pk_fma_f32 v[48:49], v[118:119], s[24:25], v[0:1] op_sel_hi:[1,1,0]
	v_pk_fma_f32 v[64:65], v[116:117], s[30:31], v[0:1] op_sel_hi:[1,1,0]
	v_pk_fma_f32 v[62:63], v[116:117], s[20:21], v[0:1] op_sel_hi:[1,1,0]
	s_waitcnt lgkmcnt(1)
	v_mfma_f32_32x32x16_bf16 v[34:49], v[50:53], v[98:101], v[34:49]
	v_fma_f32 v60, v116, s34, v0
	v_fma_f32 v61, v117, s35, v0
	v_fma_f32 v58, v116, s80, v0
	v_fma_f32 v59, v117, s81, v0
	v_fma_f32 v56, v116, s76, v0
	v_fma_f32 v57, v117, s77, v0
	v_pk_fma_f32 v[54:55], v[116:117], s[82:83], v[0:1] op_sel_hi:[1,1,0]
	v_pk_fma_f32 v[52:53], v[116:117], s[84:85], v[0:1] op_sel_hi:[1,1,0]
	v_pk_fma_f32 v[50:51], v[120:121], s[86:87], v[0:1] op_sel_hi:[1,1,0]
	v_add3_u32 v0, s10, v73, v72
	s_waitcnt lgkmcnt(0)
	v_mfma_f32_32x32x16_bf16 v[50:65], v[68:71], v[98:101], v[50:65]
	ds_read_b128 v[68:71], v0
	s_waitcnt lgkmcnt(0)
	v_mfma_f32_32x32x16_bf16 v[34:49], v[68:71], v[102:105], v[34:49]
	ds_read_b128 v[68:71], v0 offset:4096
	v_add3_u32 v0, s10, v74, v72
	s_waitcnt lgkmcnt(0)
	v_mfma_f32_32x32x16_bf16 v[50:65], v[68:71], v[102:105], v[50:65]
	ds_read_b128 v[68:71], v0
	s_waitcnt lgkmcnt(0)
	v_mfma_f32_32x32x16_bf16 v[34:49], v[68:71], v[106:109], v[34:49]
	ds_read_b128 v[68:71], v0 offset:4096
	v_add3_u32 v0, s10, v75, v72
	s_waitcnt lgkmcnt(0)
; #define LAS __attribute__((address_space(3)))
; #define MFMA32(a, b, c) __builtin_amdgcn_mfma_f32_32x32x16_bf16((a), (b), (c), 0, 0, 0)
; template <int MODE, int MK  , bool FIRST, class ValidF> ...
;     ...
;         for (int mt = 0; mt < 2; ++mt) { const bf16x8 a = *(const LAS bf16x8*)(Kb + kofs[ks] + mt * 4096); p[mt] = MFMA32(a, qf[ks], p[mt]); }
;     if (MK != 0) {
; #pragma unroll
;         for (int mt = 0; mt < 2; ++mt)
; #pragma unroll
;             for (int r = 0; r < 16; ++r) { const int kc = 32 * mt + (r & 3) + 8 * (r >> 2); const bool ok = (MK == 2) ? valid(kc + 4 * hh) : lv; p[mt][r] = ok ? p[mt][r] : -INFINITY; } }
;     if (MODE != 1) {
;         float tmax = fmaxf(p[0][0], p[1][0]);
; #pragma unroll
;         for (int r = 1; r < 16; ++r) tmax = fmaxf(tmax, fmaxf(p[0][r], p[1][r]));
;         tmax = fmaxf(tmax, __shfl_xor(tmax, 32));
;         if (MODE == 0) {
;             const float mn = fmaxf(m, tmax); const float mm = (mn == -INFINITY) ? 0.f : mn; l *= __builtin_amdgcn_exp2f(m - mm); m = mn;
; #pragma unroll
;             for (int mt = 0; mt < 2; ++mt)
; #pragma unroll
;                 for (int r = 0; r < 16; ++r) p[mt][r] -= mm;
;         } else if (FIRST) {
;             m = tmax;
; #pragma unroll
;             for (int mt = 0; mt < 2; ++mt)
; #pragma unroll
;                 for (int r = 0; r < 16; ++r) p[mt][r] -= tmax;
;         } else if (__any(tmax > 8.0f)) {
;             const float dl = fmaxf(tmax, 0.f); m += dl; const float f = __builtin_amdgcn_exp2f(-dl); l *= f;
; #pragma unroll
;             for (int mt = 0; mt < 2; ++mt)
; #pragma unroll
;                 for (int r = 0; r < 16; ++r) p[mt][r] -= dl;
; #pragma unroll
;             for (int i = 0; i < 16; ++i) { o[0][i] *= f; o[1][i] *= f; } }
	v_mfma_f32_32x32x16_bf16 v[50:65], v[68:71], v[106:109], v[50:65]
	ds_read_b128 v[68:71], v0
	s_waitcnt lgkmcnt(0)
	v_mfma_f32_32x32x16_bf16 v[34:49], v[68:71], v[110:113], v[34:49]
	ds_read_b128 v[68:71], v0 offset:4096
	s_waitcnt lgkmcnt(0)
	v_mfma_f32_32x32x16_bf16 v[50:65], v[68:71], v[110:113], v[50:65]
	s_nop 8
	v_cndmask_b32_e32 v133, v233, v35, vcc
	v_cndmask_b32_e32 v134, v233, v34, vcc
	v_cndmask_b32_e32 v132, v233, v36, vcc
	v_max_f32_e32 v34, v133, v133
	v_cndmask_b32_e32 v131, v233, v37, vcc
	v_max_f32_e32 v35, v132, v132
	v_max_f32_e32 v36, v131, v131
	v_cndmask_b32_e32 v83, v233, v51, vcc
	v_cndmask_b32_e32 v81, v233, v52, vcc
	v_max_f32_e32 v0, v83, v83
	v_cndmask_b32_e32 v80, v233, v53, vcc
	v_max_f32_e32 v0, v34, v0
	v_max_f32_e32 v34, v81, v81
	v_cndmask_b32_e32 v86, v233, v50, vcc
	v_max_f32_e32 v34, v35, v34
	v_max_f32_e32 v35, v80, v80
	v_cndmask_b32_e32 v130, v233, v38, vcc
	v_cndmask_b32_e32 v79, v233, v54, vcc
	v_max3_f32 v0, v134, v86, v0
	v_max_f32_e32 v35, v36, v35
	v_cndmask_b32_e32 v117, v233, v39, vcc
	v_cndmask_b32_e32 v78, v233, v55, vcc
	v_max3_f32 v0, v0, v34, v35
	v_max_f32_e32 v34, v79, v79
	v_max_f32_e32 v35, v130, v130
	v_max_f32_e32 v34, v35, v34
	v_max_f32_e32 v35, v78, v78
	v_max_f32_e32 v36, v117, v117
	v_cndmask_b32_e32 v97, v233, v40, vcc
	v_cndmask_b32_e32 v77, v233, v56, vcc
	v_max_f32_e32 v35, v36, v35
	v_cndmask_b32_e32 v96, v233, v41, vcc
	v_cndmask_b32_e32 v76, v233, v57, vcc
	v_max3_f32 v0, v0, v34, v35
	v_max_f32_e32 v34, v77, v77
	v_max_f32_e32 v35, v97, v97
	v_max_f32_e32 v34, v35, v34
	v_max_f32_e32 v35, v76, v76
	v_max_f32_e32 v36, v96, v96
	v_cndmask_b32_e32 v95, v233, v42, vcc
	v_cndmask_b32_e32 v75, v233, v58, vcc
	v_max_f32_e32 v35, v36, v35
	v_cndmask_b32_e32 v94, v233, v43, vcc
	v_cndmask_b32_e32 v74, v233, v59, vcc
	v_max3_f32 v0, v0, v34, v35
	v_max_f32_e32 v34, v75, v75
	v_max_f32_e32 v35, v95, v95
	v_max_f32_e32 v34, v35, v34
	v_max_f32_e32 v35, v74, v74
	v_max_f32_e32 v36, v94, v94
	v_cndmask_b32_e32 v93, v233, v44, vcc
	v_cndmask_b32_e32 v73, v233, v60, vcc
	v_max_f32_e32 v35, v36, v35
	v_cndmask_b32_e32 v92, v233, v45, vcc
	v_cndmask_b32_e32 v72, v233, v61, vcc
	v_max3_f32 v0, v0, v34, v35
	v_max_f32_e32 v34, v73, v73
	v_max_f32_e32 v35, v93, v93
	v_max_f32_e32 v34, v35, v34
	v_max_f32_e32 v35, v72, v72
	v_max_f32_e32 v36, v92, v92
	v_cndmask_b32_e32 v91, v233, v46, vcc
	v_cndmask_b32_e32 v71, v233, v62, vcc
	v_max_f32_e32 v35, v36, v35
	v_cndmask_b32_e32 v90, v233, v47, vcc
	v_cndmask_b32_e32 v70, v233, v63, vcc
	v_max3_f32 v0, v0, v34, v35
	v_max_f32_e32 v34, v71, v71
	v_max_f32_e32 v35, v91, v91
	v_max_f32_e32 v34, v35, v34
	v_max_f32_e32 v35, v70, v70
	v_max_f32_e32 v36, v90, v90
	v_cndmask_b32_e32 v89, v233, v48, vcc
	v_cndmask_b32_e32 v69, v233, v64, vcc
	v_max_f32_e32 v35, v36, v35
	v_cndmask_b32_e32 v87, v233, v49, vcc
	v_cndmask_b32_e32 v68, v233, v65, vcc
	v_max3_f32 v0, v0, v34, v35
	v_max_f32_e32 v34, v69, v69
	v_max_f32_e32 v35, v89, v89
	v_max_f32_e32 v34, v35, v34
	v_max_f32_e32 v35, v68, v68
	v_max_f32_e32 v36, v87, v87
	v_max_f32_e32 v35, v36, v35
	v_max3_f32 v0, v0, v34, v35
	v_mov_b32_e32 v34, v0
	s_nop 1
	v_permlane32_swap_b32_e32 v0, v34
	s_waitcnt lgkmcnt(0)
	v_max_f32_e32 v34, v34, v34
	v_max_f32_e32 v0, v0, v34
	v_cmp_lt_f32_e32 vcc, s74, v0
	s_cbranch_vccz .LBB0_533
	v_max_f32_e32 v0, v0, v0
	v_max_f32_e32 v35, 0, v0
	v_exp_f32_e64 v34, -v35
	v_add_f32_e32 v0, v84, v35
	v_sub_f32_e32 v134, v134, v35
	v_sub_f32_e32 v133, v133, v35
	v_mul_f32_e32 v88, v85, v34
	v_sub_f32_e32 v132, v132, v35
	v_sub_f32_e32 v131, v131, v35
	v_sub_f32_e32 v130, v130, v35
	v_sub_f32_e32 v117, v117, v35
	v_sub_f32_e32 v97, v97, v35
	v_sub_f32_e32 v96, v96, v35
	v_sub_f32_e32 v95, v95, v35
	v_sub_f32_e32 v94, v94, v35
	v_sub_f32_e32 v93, v93, v35
	v_sub_f32_e32 v92, v92, v35
	v_sub_f32_e32 v91, v91, v35
	v_sub_f32_e32 v90, v90, v35
	v_sub_f32_e32 v89, v89, v35
	v_sub_f32_e32 v87, v87, v35
	v_sub_f32_e32 v86, v86, v35
	v_sub_f32_e32 v83, v83, v35
	v_sub_f32_e32 v81, v81, v35
	v_sub_f32_e32 v80, v80, v35
	v_sub_f32_e32 v79, v79, v35
	v_sub_f32_e32 v78, v78, v35
	v_sub_f32_e32 v77, v77, v35
	v_sub_f32_e32 v76, v76, v35
	v_sub_f32_e32 v75, v75, v35
	v_sub_f32_e32 v74, v74, v35
	v_sub_f32_e32 v73, v73, v35
	v_sub_f32_e32 v72, v72, v35
	v_sub_f32_e32 v71, v71, v35
	v_sub_f32_e32 v70, v70, v35
	v_sub_f32_e32 v69, v69, v35
	v_sub_f32_e32 v68, v68, v35
	v_pk_mul_f32 v[64:65], v[32:33], v[34:35] op_sel_hi:[1,0]
	v_pk_mul_f32 v[62:63], v[30:31], v[34:35] op_sel_hi:[1,0]
	v_pk_mul_f32 v[60:61], v[28:29], v[34:35] op_sel_hi:[1,0]
	v_pk_mul_f32 v[58:59], v[26:27], v[34:35] op_sel_hi:[1,0]
	v_pk_mul_f32 v[56:57], v[24:25], v[34:35] op_sel_hi:[1,0]
	v_pk_mul_f32 v[54:55], v[22:23], v[34:35] op_sel_hi:[1,0]
	v_pk_mul_f32 v[52:53], v[20:21], v[34:35] op_sel_hi:[1,0]
	v_pk_mul_f32 v[50:51], v[18:19], v[34:35] op_sel_hi:[1,0]
	v_pk_mul_f32 v[48:49], v[16:17], v[34:35] op_sel_hi:[1,0]
	v_pk_mul_f32 v[46:47], v[14:15], v[34:35] op_sel_hi:[1,0]
	v_pk_mul_f32 v[44:45], v[12:13], v[34:35] op_sel_hi:[1,0]
	v_pk_mul_f32 v[42:43], v[10:11], v[34:35] op_sel_hi:[1,0]
	v_pk_mul_f32 v[40:41], v[8:9], v[34:35] op_sel_hi:[1,0]
	v_pk_mul_f32 v[38:39], v[6:7], v[34:35] op_sel_hi:[1,0]
	v_pk_mul_f32 v[36:37], v[4:5], v[34:35] op_sel_hi:[1,0]
	v_pk_mul_f32 v[34:35], v[2:3], v[34:35] op_sel_hi:[1,0]
	s_branch .LBB0_534

; #define LAS __attribute__((address_space(3)))
; #define MFMA32(a, b, c) __builtin_amdgcn_mfma_f32_32x32x16_bf16((a), (b), (c), 0, 0, 0)
; template <int MODE, int MK  , bool FIRST, class ValidF> ...
;     ...
;     const float cref = c0 + sbk * (float)(4 * hh) - ((MODE == 2 && !FIRST) || MODE == 1 ? m : 0.f);
; #pragma unroll
;     for (int mt = 0; mt < 2; ++mt)
; #pragma unroll
;         for (int r = 0; r < 16; ++r) p[mt][r] = fmaf(sbk, (float)(32 * mt + (r & 3) + 8 * (r >> 2)), cref);
; #pragma unroll
;     for (int ks = 0; ks < 4; ++ks)
; #pragma unroll
;         for (int mt = 0; mt < 2; ++mt) { const bf16x8 a = *(const LAS bf16x8*)(Kb + kofs[ks] + mt * 4096); p[mt] = MFMA32(a, qf[ks], p[mt]); }
;     if (MK != 0) {
; #pragma unroll
;         for (int mt = 0; mt < 2; ++mt)
; #pragma unroll
;             for (int r = 0; r < 16; ++r) { const int kc = 32 * mt + (r & 3) + 8 * (r >> 2); const bool ok = (MK == 2) ? valid(kc + 4 * hh) : lv; p[mt][r] = ok ? p[mt][r] : -INFINITY; } }
;     if (MODE != 1) {
;         float tmax = fmaxf(p[0][0], p[1][0]);
; #pragma unroll
;         for (int r = 1; r < 16; ++r) tmax = fmaxf(tmax, fmaxf(p[0][r], p[1][r]));
;         tmax = fmaxf(tmax, __shfl_xor(tmax, 32));
;         if (MODE == 0) {
;             const float mn = fmaxf(m, tmax); const float mm = (mn == -INFINITY) ? 0.f : mn; l *= __builtin_amdgcn_exp2f(m - mm); m = mn;
; #pragma unroll
;             for (int mt = 0; mt < 2; ++mt)
; #pragma unroll
;                 for (int r = 0; r < 16; ++r) p[mt][r] -= mm;
;         } else if (FIRST) {
;             m = tmax;
; #pragma unroll
;             for (int mt = 0; mt < 2; ++mt)
; #pragma unroll
;                 for (int r = 0; r < 16; ++r) p[mt][r] -= tmax;
;         } else if (__any(tmax > 8.0f)) {
;             const float dl = fmaxf(tmax, 0.f); m += dl; const float f = __builtin_amdgcn_exp2f(-dl); l *= f;
; #pragma unroll
;             for (int mt = 0; mt < 2; ++mt)
; #pragma unroll
;                 for (int r = 0; r < 16; ++r) p[mt][r] -= dl;
; #pragma unroll
;             for (int i = 0; i < 16; ++i) { o[0][i] *= f; o[1][i] *= f; } }
.LBB0_535:
	s_and_b64 vcc, exec, s[0:1]
	s_cbranch_vccz .LBB0_539
	v_mov_b32_e32 v0, v123
	v_mov_b32_e32 v117, v116
	v_ashrrev_i32_e32 v67, 5, v0
	v_lshlrev_b32_e32 v66, 2, v67
	v_lshlrev_b32_e32 v34, 7, v0
	v_cvt_f32_i32_e32 v35, v66
	v_and_b32_e32 v73, 0xf80, v34
	v_bitop3_b32 v34, v67, v0, 7 bitop3:0x78
	v_lshlrev_b32_e32 v34, 4, v34
	v_add_u32_e32 v36, 2, v67
	v_bitop3_b32 v36, v36, v0, 7 bitop3:0x78
	v_add3_u32 v38, s10, v34, v73
	v_lshlrev_b32_e32 v74, 4, v36
	v_fmac_f32_e32 v82, v116, v35
	ds_read_b128 v[34:37], v38
	ds_read_b128 v[68:71], v38 offset:4096
	v_sub_f32_e32 v72, v82, v84
	v_fma_f32 v50, 0, v116, v72
	v_add_f32_e32 v51, v116, v72
	v_pk_fma_f32 v[52:53], v[118:119], s[18:19], v[72:73] op_sel_hi:[1,1,0]
	v_pk_fma_f32 v[54:55], v[118:119], s[74:75], v[72:73] op_sel_hi:[1,1,0]
	v_pk_fma_f32 v[56:57], v[118:119], s[36:37], v[72:73] op_sel_hi:[1,1,0]
	v_pk_fma_f32 v[58:59], v[118:119], s[26:27], v[72:73] op_sel_hi:[1,1,0]
	v_pk_fma_f32 v[60:61], v[118:119], s[56:57], v[72:73] op_sel_hi:[1,1,0]
	v_pk_fma_f32 v[62:63], v[118:119], s[22:23], v[72:73] op_sel_hi:[1,1,0]
	v_pk_fma_f32 v[64:65], v[118:119], s[24:25], v[72:73] op_sel_hi:[1,1,0]
	v_pk_fma_f32 v[48:49], v[116:117], s[30:31], v[72:73] op_sel_hi:[1,1,0]
	v_pk_fma_f32 v[46:47], v[116:117], s[20:21], v[72:73] op_sel_hi:[1,1,0]
	s_waitcnt lgkmcnt(1)
	v_mfma_f32_32x32x16_bf16 v[50:65], v[34:37], v[98:101], v[50:65]
	v_fma_f32 v44, v116, s34, v72
	v_fma_f32 v45, v117, s35, v72
	v_fma_f32 v42, v116, s80, v72
	v_fma_f32 v43, v117, s81, v72
	v_fma_f32 v40, v116, s76, v72
	v_fma_f32 v41, v117, s77, v72
	v_pk_fma_f32 v[38:39], v[116:117], s[82:83], v[72:73] op_sel_hi:[1,1,0]
	v_pk_fma_f32 v[36:37], v[116:117], s[84:85], v[72:73] op_sel_hi:[1,1,0]
	v_pk_fma_f32 v[34:35], v[120:121], s[86:87], v[72:73] op_sel_hi:[1,1,0]
	v_add3_u32 v72, s10, v74, v73
	s_waitcnt lgkmcnt(0)
	v_mfma_f32_32x32x16_bf16 v[34:49], v[68:71], v[98:101], v[34:49]
	ds_read_b128 v[68:71], v72
	s_waitcnt lgkmcnt(0)
	v_mfma_f32_32x32x16_bf16 v[50:65], v[68:71], v[102:105], v[50:65]
	ds_read_b128 v[68:71], v72 offset:4096
	v_add_u32_e32 v72, 4, v67
	v_bitop3_b32 v72, v72, v0, 7 bitop3:0x78
	v_lshlrev_b32_e32 v72, 4, v72
	v_add3_u32 v72, s10, v72, v73
	v_add_u32_e32 v67, 6, v67
	v_bitop3_b32 v67, v67, v0, 7 bitop3:0x78
	s_waitcnt lgkmcnt(0)
	v_mfma_f32_32x32x16_bf16 v[34:49], v[68:71], v[102:105], v[34:49]
	ds_read_b128 v[68:71], v72
	v_lshlrev_b32_e32 v67, 4, v67
	v_add3_u32 v67, s10, v67, v73
	s_waitcnt lgkmcnt(0)
	v_mfma_f32_32x32x16_bf16 v[50:65], v[68:71], v[106:109], v[50:65]
	ds_read_b128 v[68:71], v72 offset:4096
	s_waitcnt lgkmcnt(0)
	v_mfma_f32_32x32x16_bf16 v[34:49], v[68:71], v[106:109], v[34:49]
	ds_read_b128 v[68:71], v67 offset:4096
	s_waitcnt lgkmcnt(0)
	v_mfma_f32_32x32x16_bf16 v[34:49], v[68:71], v[110:113], v[34:49]
	ds_read_b128 v[68:71], v67
	s_waitcnt lgkmcnt(0)
	v_mfma_f32_32x32x16_bf16 v[50:65], v[68:71], v[110:113], v[50:65]
	s_nop 8
	v_max_f32_e32 v67, v35, v35
	s_nop 1
	v_max_f32_e32 v68, v51, v51
	v_max_f32_e32 v67, v68, v67
	v_max_f32_e32 v68, v36, v36
	v_max_f32_e32 v69, v52, v52
	v_max_f32_e32 v68, v69, v68
	v_max_f32_e32 v69, v37, v37
	v_max_f32_e32 v70, v53, v53
	v_max3_f32 v67, v50, v34, v67
	v_max_f32_e32 v69, v70, v69
	v_max3_f32 v67, v67, v68, v69
	v_max_f32_e32 v68, v38, v38
	v_max_f32_e32 v69, v54, v54
	v_max_f32_e32 v68, v69, v68
	v_max_f32_e32 v69, v39, v39
	v_max_f32_e32 v70, v55, v55
	v_max_f32_e32 v69, v70, v69
	v_max3_f32 v67, v67, v68, v69
	v_max_f32_e32 v68, v40, v40
	v_max_f32_e32 v69, v56, v56
	v_max_f32_e32 v68, v69, v68
	v_max_f32_e32 v69, v41, v41
	v_max_f32_e32 v70, v57, v57
	v_max_f32_e32 v69, v70, v69
	v_max3_f32 v67, v67, v68, v69
	v_max_f32_e32 v68, v42, v42
	v_max_f32_e32 v69, v58, v58
	v_max_f32_e32 v68, v69, v68
	v_max_f32_e32 v69, v43, v43
	v_max_f32_e32 v70, v59, v59
	v_max_f32_e32 v69, v70, v69
	v_max3_f32 v67, v67, v68, v69
	v_max_f32_e32 v68, v44, v44
	v_max_f32_e32 v69, v60, v60
	v_max_f32_e32 v68, v69, v68
	v_max_f32_e32 v69, v45, v45
	v_max_f32_e32 v70, v61, v61
	v_max_f32_e32 v69, v70, v69
	v_max3_f32 v67, v67, v68, v69
	v_max_f32_e32 v68, v46, v46
	v_max_f32_e32 v69, v62, v62
	v_max_f32_e32 v68, v69, v68
	v_max_f32_e32 v69, v47, v47
	v_max_f32_e32 v70, v63, v63
	v_max_f32_e32 v69, v70, v69
	v_max3_f32 v67, v67, v68, v69
	v_max_f32_e32 v68, v48, v48
	v_max_f32_e32 v69, v64, v64
	v_max_f32_e32 v68, v69, v68
	v_max_f32_e32 v69, v49, v49
	v_max_f32_e32 v70, v65, v65
	v_max_f32_e32 v69, v70, v69
	v_max3_f32 v67, v67, v68, v69
	v_mov_b32_e32 v68, v67
	s_nop 1
	v_permlane32_swap_b32_e32 v67, v68
	s_waitcnt lgkmcnt(0)
	v_max_f32_e32 v68, v68, v68
	v_max_f32_e32 v67, v67, v68
	v_cmp_lt_f32_e32 vcc, s74, v67
	s_cbranch_vccz .LBB0_538
	v_max_f32_e32 v67, v67, v67
	v_max_f32_e32 v67, 0, v67
	v_exp_f32_e64 v68, -v67
	v_add_f32_e32 v84, v84, v67
	v_sub_f32_e32 v50, v50, v67
	v_sub_f32_e32 v51, v51, v67
	v_mul_f32_e32 v85, v85, v68
	v_sub_f32_e32 v52, v52, v67
	v_sub_f32_e32 v53, v53, v67
	v_sub_f32_e32 v54, v54, v67
	v_sub_f32_e32 v55, v55, v67
	v_sub_f32_e32 v56, v56, v67
	v_sub_f32_e32 v57, v57, v67
	v_sub_f32_e32 v58, v58, v67
	v_sub_f32_e32 v59, v59, v67
	v_sub_f32_e32 v60, v60, v67
	v_sub_f32_e32 v61, v61, v67
	v_sub_f32_e32 v62, v62, v67
	v_sub_f32_e32 v63, v63, v67
	v_sub_f32_e32 v64, v64, v67
	v_sub_f32_e32 v65, v65, v67
	v_sub_f32_e32 v34, v34, v67
	v_sub_f32_e32 v35, v35, v67
	v_sub_f32_e32 v36, v36, v67
	v_sub_f32_e32 v37, v37, v67
	v_sub_f32_e32 v38, v38, v67
	v_sub_f32_e32 v39, v39, v67
	v_sub_f32_e32 v40, v40, v67
	v_sub_f32_e32 v41, v41, v67
	v_sub_f32_e32 v42, v42, v67
	v_sub_f32_e32 v43, v43, v67
	v_sub_f32_e32 v44, v44, v67
	v_sub_f32_e32 v45, v45, v67
	v_sub_f32_e32 v46, v46, v67
	v_sub_f32_e32 v47, v47, v67
	v_sub_f32_e32 v48, v48, v67
	v_sub_f32_e32 v49, v49, v67
	v_pk_mul_f32 v[32:33], v[32:33], v[68:69] op_sel_hi:[1,0]
	v_pk_mul_f32 v[30:31], v[30:31], v[68:69] op_sel_hi:[1,0]
	v_pk_mul_f32 v[28:29], v[28:29], v[68:69] op_sel_hi:[1,0]
	v_pk_mul_f32 v[26:27], v[26:27], v[68:69] op_sel_hi:[1,0]
	v_pk_mul_f32 v[24:25], v[24:25], v[68:69] op_sel_hi:[1,0]
	v_pk_mul_f32 v[22:23], v[22:23], v[68:69] op_sel_hi:[1,0]
	v_pk_mul_f32 v[20:21], v[20:21], v[68:69] op_sel_hi:[1,0]
	v_pk_mul_f32 v[18:19], v[18:19], v[68:69] op_sel_hi:[1,0]
	v_pk_mul_f32 v[16:17], v[16:17], v[68:69] op_sel_hi:[1,0]
	v_pk_mul_f32 v[14:15], v[14:15], v[68:69] op_sel_hi:[1,0]
	v_pk_mul_f32 v[12:13], v[12:13], v[68:69] op_sel_hi:[1,0]
	v_pk_mul_f32 v[10:11], v[10:11], v[68:69] op_sel_hi:[1,0]
	v_pk_mul_f32 v[8:9], v[8:9], v[68:69] op_sel_hi:[1,0]
	v_pk_mul_f32 v[6:7], v[6:7], v[68:69] op_sel_hi:[1,0]
	v_pk_mul_f32 v[4:5], v[4:5], v[68:69] op_sel_hi:[1,0]
	v_pk_mul_f32 v[2:3], v[2:3], v[68:69] op_sel_hi:[1,0]

; template <int MODE, int MK  , bool FIRST, class ValidF> ...
;     ...
;     const float cref = c0 + sbk * (float)(4 * hh) - ((MODE == 2 && !FIRST) || MODE == 1 ? m : 0.f);
; #pragma unroll
;     for (int mt = 0; mt < 2; ++mt)
; #pragma unroll
;         for (int r = 0; r < 16; ++r) p[mt][r] = fmaf(sbk, (float)(32 * mt + (r & 3) + 8 * (r >> 2)), cref);
; #pragma unroll
;     for (int ks = 0; ks < 4; ++ks)
; #pragma unroll
;         for (int mt = 0; mt < 2; ++mt) { const bf16x8 a = *(const LAS bf16x8*)(Kb + kofs[ks] + mt * 4096); p[mt] = MFMA32(a, qf[ks], p[mt]); }
;     if (MK != 0) {
; #pragma unroll
;         for (int mt = 0; mt < 2; ++mt)
; #pragma unroll
;             for (int r = 0; r < 16; ++r) { const int kc = 32 * mt + (r & 3) + 8 * (r >> 2); const bool ok = (MK == 2) ? valid(kc + 4 * hh) : lv; p[mt][r] = ok ? p[mt][r] : -INFINITY; } }
;     if (MODE != 1) {
;         float tmax = fmaxf(p[0][0], p[1][0]);
; #pragma unroll
; __device__ __forceinline__ void nsa_mfma_phase(Frame& F, int l, bf16* YC, int ypitch) {
;     ...
;             for (;;) {
;                 if (j - 1 >= jlast) NSA_WAIT_BAR(2); else NSA_WAIT_BAR(0);
;                 if (j - 2 >= jlast) { const int s2 = slot >= 1 ? slot - 1 : 2; NSA_ISSUE(s2, zb + (size_t)(64 * (j - 2)) * NZ + Z_KW + g * 64, zb + (size_t)(64 * (j - 2)) * NZ + Z_VW + g * 64, loffZ); }
;                 bool livew = true;
;                 if (j != c) { const float bound = ((LAS float*)(lds + L_QN))[w * 64 + lane] * ((LAS float*)(lds + L_KMX))[64 + j] + slope2 * (float)(64 * (j - c) + 63) - m; livew = !__all(bound < -40.0f); }
;                 if (livew) { const int dj = 64 * (c - j); int tq = L.tq; asm volatile("" : "+v"(tq));
;                     auto valid = [&](int koff) { return (dj + tq - koff >= 0) && (dj + tq - koff <= WIN - 1); };
;                     const LAS unsigned char* Kb = lds + L_K + slot * TB; const LAS unsigned char* Vb = lds + L_V + slot * TB;
;                     if (j == c) tile_compute<2, 2, true>(Kb, Vb, qf, slope2 * (float)(64 * (j - c)), slope2, true, valid, m, lsum, o, IMP, L);
;                     else if (j == c - 8) tile_compute<2, 2, false>(Kb, Vb, qf, slope2 * (float)(64 * (j - c)), slope2, true, valid, m, lsum, o, IMP, L);
;                     else tile_compute<2, 0, false>(Kb, Vb, qf, slope2 * (float)(64 * (j - c)), slope2, true, valid, m, lsum, o, IMP, L); }
.LBB0_555:
	s_andn2_b64 vcc, exec, s[2:3]
	s_cbranch_vccnz .LBB0_548
	s_lshl_b32 s2, s45, 13
	v_mov_b32_e32 v0, v124
	s_add_i32 s58, s2, 0
	s_mov_b64 s[2:3], -1
	s_and_b64 vcc, exec, s[0:1]
	s_cbranch_vccz .LBB0_567
	s_cmpk_lg_i32 s13, 0x1c5
	s_mov_b64 s[0:1], -1
	s_cbranch_scc0 .LBB0_561
	v_mov_b32_e32 v133, v123
	s_lshl_b32 s0, s10, 6
	v_ashrrev_i32_e32 v43, 5, v133
	v_lshlrev_b32_e32 v34, 7, v133
	v_and_b32_e32 v44, 0xf80, v34
	v_bitop3_b32 v34, v43, v133, 7 bitop3:0x78
	v_lshlrev_b32_e32 v134, 2, v43
	v_lshlrev_b32_e32 v36, 4, v34
	v_cvt_f32_i32_e32 v34, s0
	v_cvt_f32_i32_e32 v35, v134
	v_add_u32_e32 v37, 2, v43
	v_bitop3_b32 v37, v37, v133, 7 bitop3:0x78
	v_add3_u32 v38, s58, v36, v44
	v_pk_mul_f32 v[34:35], v[118:119], v[34:35]
	v_lshlrev_b32_e32 v45, 4, v37
	v_add_f32_e32 v34, v34, v35
	v_sub_f32_e32 v42, v34, v132
	ds_read_b128 v[34:37], v38
	ds_read_b128 v[38:41], v38 offset:4096
	v_fma_f32 v82, 0, v116, v42
	v_add_f32_e32 v83, v116, v42
	v_pk_fma_f32 v[84:85], v[118:119], s[18:19], v[42:43] op_sel_hi:[1,1,0]
	v_pk_fma_f32 v[86:87], v[118:119], s[74:75], v[42:43] op_sel_hi:[1,1,0]
	v_pk_fma_f32 v[88:89], v[118:119], s[36:37], v[42:43] op_sel_hi:[1,1,0]
	v_pk_fma_f32 v[90:91], v[118:119], s[26:27], v[42:43] op_sel_hi:[1,1,0]
	v_pk_fma_f32 v[92:93], v[118:119], s[56:57], v[42:43] op_sel_hi:[1,1,0]
	v_pk_fma_f32 v[94:95], v[118:119], s[22:23], v[42:43] op_sel_hi:[1,1,0]
	v_pk_fma_f32 v[96:97], v[118:119], s[24:25], v[42:43] op_sel_hi:[1,1,0]
	v_mov_b32_e32 v117, v116
	v_pk_fma_f32 v[80:81], v[116:117], s[30:31], v[42:43] op_sel_hi:[1,1,0]
	s_waitcnt lgkmcnt(1)
	v_mfma_f32_32x32x16_bf16 v[82:97], v[34:37], v[98:101], v[82:97]
	v_fma_f32 v78, v116, s20, v42
	v_fma_f32 v79, v117, s21, v42
	v_fma_f32 v76, v116, s34, v42
	v_fma_f32 v77, v117, s35, v42
	v_fma_f32 v74, v116, s80, v42
	v_fma_f32 v75, v117, s81, v42
	v_pk_fma_f32 v[72:73], v[116:117], s[76:77], v[42:43] op_sel_hi:[1,1,0]
	v_pk_fma_f32 v[70:71], v[116:117], s[82:83], v[42:43] op_sel_hi:[1,1,0]
	v_pk_fma_f32 v[68:69], v[116:117], s[84:85], v[42:43] op_sel_hi:[1,1,0]
	v_pk_fma_f32 v[66:67], v[120:121], s[86:87], v[42:43] op_sel_hi:[1,1,0]
	v_mov_b32_e32 v135, v131
	v_mov_b32_e32 v117, v132
	s_waitcnt lgkmcnt(0)
	v_mfma_f32_32x32x16_bf16 v[66:81], v[38:41], v[98:101], v[66:81]
	v_add3_u32 v38, s58, v45, v44
	ds_read_b128 v[34:37], v38
	ds_read_b128 v[38:41], v38 offset:4096
	s_waitcnt lgkmcnt(1)
	v_mfma_f32_32x32x16_bf16 v[82:97], v[34:37], v[102:105], v[82:97]
	v_add_u32_e32 v34, 4, v43
	v_bitop3_b32 v34, v34, v133, 7 bitop3:0x78
	v_lshlrev_b32_e32 v34, 4, v34
	s_waitcnt lgkmcnt(0)
	v_mfma_f32_32x32x16_bf16 v[66:81], v[38:41], v[102:105], v[66:81]
	v_add3_u32 v38, s58, v34, v44
	ds_read_b128 v[34:37], v38
	ds_read_b128 v[38:41], v38 offset:4096
	s_waitcnt lgkmcnt(1)
	v_mfma_f32_32x32x16_bf16 v[82:97], v[34:37], v[106:109], v[82:97]
	v_add_u32_e32 v34, 6, v43
	v_bitop3_b32 v34, v34, v133, 7 bitop3:0x78
	v_lshlrev_b32_e32 v34, 4, v34
	s_waitcnt lgkmcnt(0)
	v_mfma_f32_32x32x16_bf16 v[66:81], v[38:41], v[106:109], v[66:81]
	v_add3_u32 v38, s58, v34, v44
	ds_read_b128 v[34:37], v38 offset:4096
	ds_read_b128 v[38:41], v38
	s_waitcnt lgkmcnt(1)
	v_mfma_f32_32x32x16_bf16 v[66:81], v[34:37], v[110:113], v[66:81]
	s_waitcnt lgkmcnt(0)
	v_mfma_f32_32x32x16_bf16 v[82:97], v[38:41], v[110:113], v[82:97]
	s_nop 9
	v_max_f32_e32 v34, v67, v67
	s_nop 0
	v_max_f32_e32 v35, v83, v83
	v_max_f32_e32 v34, v35, v34
	v_max_f32_e32 v35, v68, v68
	v_max_f32_e32 v36, v84, v84
	v_max_f32_e32 v35, v36, v35
	v_max_f32_e32 v36, v69, v69
	v_max_f32_e32 v37, v85, v85
	v_max3_f32 v34, v82, v66, v34
	v_max_f32_e32 v36, v37, v36
	v_max3_f32 v34, v34, v35, v36
	v_max_f32_e32 v35, v70, v70
	v_max_f32_e32 v36, v86, v86
	v_max_f32_e32 v35, v36, v35
	v_max_f32_e32 v36, v71, v71
	v_max_f32_e32 v37, v87, v87
	v_max_f32_e32 v36, v37, v36
	v_max3_f32 v34, v34, v35, v36
	v_max_f32_e32 v35, v72, v72
	v_max_f32_e32 v36, v88, v88
	v_max_f32_e32 v35, v36, v35
	v_max_f32_e32 v36, v73, v73
	v_max_f32_e32 v37, v89, v89
	v_max_f32_e32 v36, v37, v36
	v_max3_f32 v34, v34, v35, v36
	v_max_f32_e32 v35, v74, v74
	v_max_f32_e32 v36, v90, v90
	v_max_f32_e32 v35, v36, v35
	v_max_f32_e32 v36, v75, v75
	v_max_f32_e32 v37, v91, v91
	v_max_f32_e32 v36, v37, v36
	v_max3_f32 v34, v34, v35, v36
	v_max_f32_e32 v35, v76, v76
	v_max_f32_e32 v36, v92, v92
	v_max_f32_e32 v35, v36, v35
	v_max_f32_e32 v36, v77, v77
	v_max_f32_e32 v37, v93, v93
	v_max_f32_e32 v36, v37, v36
	v_max3_f32 v34, v34, v35, v36
	v_max_f32_e32 v35, v78, v78
	v_max_f32_e32 v36, v94, v94
	v_max_f32_e32 v35, v36, v35
	v_max_f32_e32 v36, v79, v79
	v_max_f32_e32 v37, v95, v95
	v_max_f32_e32 v36, v37, v36
	v_max3_f32 v34, v34, v35, v36
	v_max_f32_e32 v35, v80, v80
	v_max_f32_e32 v36, v96, v96
	v_max_f32_e32 v35, v36, v35
	v_max_f32_e32 v36, v81, v81
	v_max_f32_e32 v37, v97, v97
	v_max_f32_e32 v36, v37, v36
	v_max3_f32 v34, v34, v35, v36
	v_mov_b32_e32 v35, v34
	s_nop 1
	v_permlane32_swap_b32_e32 v34, v35
	s_waitcnt lgkmcnt(0)
	v_max_f32_e32 v35, v35, v35
	v_max_f32_e32 v136, v34, v35
	v_mov_b64_e32 v[64:65], v[32:33]
	v_cmp_lt_f32_e32 vcc, s74, v136
	v_mov_b64_e32 v[62:63], v[30:31]
	v_mov_b64_e32 v[60:61], v[28:29]
	v_mov_b64_e32 v[58:59], v[26:27]
	v_mov_b64_e32 v[56:57], v[24:25]
	v_mov_b64_e32 v[54:55], v[22:23]
	v_mov_b64_e32 v[52:53], v[20:21]
	v_mov_b64_e32 v[50:51], v[18:19]
	v_mov_b64_e32 v[48:49], v[16:17]
	v_mov_b64_e32 v[46:47], v[14:15]
	v_mov_b64_e32 v[44:45], v[12:13]
	v_mov_b64_e32 v[42:43], v[10:11]
	v_mov_b64_e32 v[40:41], v[8:9]
	v_mov_b64_e32 v[38:39], v[6:7]
	v_mov_b64_e32 v[36:37], v[4:5]
	v_mov_b64_e32 v[34:35], v[2:3]
	s_cbranch_vccz .LBB0_560
; template <int MODE, int MK  , bool FIRST, class ValidF> ...
;     ...
;         } else if (__any(tmax > 8.0f)) {
;             const float dl = fmaxf(tmax, 0.f); m += dl; const float f = __builtin_amdgcn_exp2f(-dl); l *= f;
; #pragma unroll
;             for (int mt = 0; mt < 2; ++mt)
; #pragma unroll
;                 for (int r = 0; r < 16; ++r) p[mt][r] -= dl;
; #pragma unroll
;             for (int i = 0; i < 16; ++i) { o[0][i] *= f; o[1][i] *= f; } }
	v_max_f32_e32 v34, v136, v136
	v_max_f32_e32 v35, 0, v34
	v_exp_f32_e64 v34, -v35
	v_add_f32_e32 v117, v132, v35
	v_sub_f32_e32 v82, v82, v35
	v_sub_f32_e32 v83, v83, v35
	v_mul_f32_e32 v135, v131, v34
	v_sub_f32_e32 v84, v84, v35
	v_sub_f32_e32 v85, v85, v35
	v_sub_f32_e32 v86, v86, v35
	v_sub_f32_e32 v87, v87, v35
	v_sub_f32_e32 v88, v88, v35
	v_sub_f32_e32 v89, v89, v35
	v_sub_f32_e32 v90, v90, v35
	v_sub_f32_e32 v91, v91, v35
	v_sub_f32_e32 v92, v92, v35
	v_sub_f32_e32 v93, v93, v35
	v_sub_f32_e32 v94, v94, v35
	v_sub_f32_e32 v95, v95, v35
	v_sub_f32_e32 v96, v96, v35
	v_sub_f32_e32 v97, v97, v35
	v_sub_f32_e32 v66, v66, v35
	v_sub_f32_e32 v67, v67, v35
	v_sub_f32_e32 v68, v68, v35
	v_sub_f32_e32 v69, v69, v35
	v_sub_f32_e32 v70, v70, v35
	v_sub_f32_e32 v71, v71, v35
	v_sub_f32_e32 v72, v72, v35
	v_sub_f32_e32 v73, v73, v35
	v_sub_f32_e32 v74, v74, v35
	v_sub_f32_e32 v75, v75, v35
	v_sub_f32_e32 v76, v76, v35
	v_sub_f32_e32 v77, v77, v35
	v_sub_f32_e32 v78, v78, v35
	v_sub_f32_e32 v79, v79, v35
	v_sub_f32_e32 v80, v80, v35
	v_sub_f32_e32 v81, v81, v35
	v_pk_mul_f32 v[64:65], v[32:33], v[34:35] op_sel_hi:[1,0]
	v_pk_mul_f32 v[62:63], v[30:31], v[34:35] op_sel_hi:[1,0]
	v_pk_mul_f32 v[60:61], v[28:29], v[34:35] op_sel_hi:[1,0]
	v_pk_mul_f32 v[58:59], v[26:27], v[34:35] op_sel_hi:[1,0]
	v_pk_mul_f32 v[56:57], v[24:25], v[34:35] op_sel_hi:[1,0]
	v_pk_mul_f32 v[54:55], v[22:23], v[34:35] op_sel_hi:[1,0]
	v_pk_mul_f32 v[52:53], v[20:21], v[34:35] op_sel_hi:[1,0]
	v_pk_mul_f32 v[50:51], v[18:19], v[34:35] op_sel_hi:[1,0]
	v_pk_mul_f32 v[48:49], v[16:17], v[34:35] op_sel_hi:[1,0]
	v_pk_mul_f32 v[46:47], v[14:15], v[34:35] op_sel_hi:[1,0]
	v_pk_mul_f32 v[44:45], v[12:13], v[34:35] op_sel_hi:[1,0]
	v_pk_mul_f32 v[42:43], v[10:11], v[34:35] op_sel_hi:[1,0]
	v_pk_mul_f32 v[40:41], v[8:9], v[34:35] op_sel_hi:[1,0]
	v_pk_mul_f32 v[38:39], v[6:7], v[34:35] op_sel_hi:[1,0]
	v_pk_mul_f32 v[36:37], v[4:5], v[34:35] op_sel_hi:[1,0]
	v_pk_mul_f32 v[34:35], v[2:3], v[34:35] op_sel_hi:[1,0]

; #define LAS __attribute__((address_space(3)))
; #define MFMA32(a, b, c) __builtin_amdgcn_mfma_f32_32x32x16_bf16((a), (b), (c), 0, 0, 0)
; template <int MODE, int MK  , bool FIRST, class ValidF> ...
;     ...
;     const float cref = c0 + sbk * (float)(4 * hh) - ((MODE == 2 && !FIRST) || MODE == 1 ? m : 0.f);
; #pragma unroll
;     for (int mt = 0; mt < 2; ++mt)
; #pragma unroll
;         for (int r = 0; r < 16; ++r) p[mt][r] = fmaf(sbk, (float)(32 * mt + (r & 3) + 8 * (r >> 2)), cref);
; #pragma unroll
;     for (int ks = 0; ks < 4; ++ks)
; #pragma unroll
;         for (int mt = 0; mt < 2; ++mt) { const bf16x8 a = *(const LAS bf16x8*)(Kb + kofs[ks] + mt * 4096); p[mt] = MFMA32(a, qf[ks], p[mt]); }
;     if (MK != 0) {
; #pragma unroll
;         for (int mt = 0; mt < 2; ++mt)
; #pragma unroll
;             for (int r = 0; r < 16; ++r) { const int kc = 32 * mt + (r & 3) + 8 * (r >> 2); const bool ok = (MK == 2) ? valid(kc + 4 * hh) : lv; p[mt][r] = ok ? p[mt][r] : -INFINITY; } }
; __device__ __forceinline__ void nsa_mfma_phase(Frame& F, int l, bf16* YC, int ypitch) {
;     ...
;                     auto valid = [&](int koff) { return (dj + tq - koff >= 0) && (dj + tq - koff <= WIN - 1); };
;                     const LAS unsigned char* Kb = lds + L_K + slot * TB; const LAS unsigned char* Vb = lds + L_V + slot * TB;
;                     if (j == c) tile_compute<2, 2, true>(Kb, Vb, qf, slope2 * (float)(64 * (j - c)), slope2, true, valid, m, lsum, o, IMP, L);
;                     else if (j == c - 8) tile_compute<2, 2, false>(Kb, Vb, qf, slope2 * (float)(64 * (j - c)), slope2, true, valid, m, lsum, o, IMP, L);
.LBB0_561:
	s_and_b64 vcc, exec, s[0:1]
	s_cbranch_vccz .LBB0_566
	v_mov_b32_e32 v94, v123
	v_mov_b32_e32 v117, v116
	v_ashrrev_i32_e32 v74, 5, v94
	v_lshlrev_b32_e32 v95, 2, v74
	v_cvt_f32_i32_e32 v35, v95
	v_lshlrev_b32_e32 v34, 7, v94
	v_and_b32_e32 v75, 0xf80, v34
	v_bitop3_b32 v34, v74, v94, 7 bitop3:0x78
	v_lshlrev_b32_e32 v34, 4, v34
	v_add_u32_e32 v36, 2, v74
	v_bitop3_b32 v36, v36, v94, 7 bitop3:0x78
	v_fma_f32 v35, v116, v35, -v130
	v_add3_u32 v38, s58, v34, v75
	v_lshlrev_b32_e32 v71, 4, v36
	v_sub_f32_e32 v70, v35, v132
	ds_read_b128 v[34:37], v38
	ds_read_b128 v[66:69], v38 offset:4096
	v_fma_f32 v50, 0, v116, v70
	v_add_f32_e32 v51, v116, v70
	v_pk_fma_f32 v[52:53], v[118:119], s[18:19], v[70:71] op_sel_hi:[1,1,0]
	v_pk_fma_f32 v[54:55], v[118:119], s[74:75], v[70:71] op_sel_hi:[1,1,0]
	v_pk_fma_f32 v[56:57], v[118:119], s[36:37], v[70:71] op_sel_hi:[1,1,0]
	v_pk_fma_f32 v[58:59], v[118:119], s[26:27], v[70:71] op_sel_hi:[1,1,0]
	v_pk_fma_f32 v[60:61], v[118:119], s[56:57], v[70:71] op_sel_hi:[1,1,0]
	v_pk_fma_f32 v[62:63], v[118:119], s[22:23], v[70:71] op_sel_hi:[1,1,0]
	v_pk_fma_f32 v[64:65], v[118:119], s[24:25], v[70:71] op_sel_hi:[1,1,0]
	v_pk_fma_f32 v[48:49], v[116:117], s[30:31], v[70:71] op_sel_hi:[1,1,0]
	v_pk_fma_f32 v[46:47], v[116:117], s[20:21], v[70:71] op_sel_hi:[1,1,0]
	s_waitcnt lgkmcnt(1)
	v_mfma_f32_32x32x16_bf16 v[50:65], v[34:37], v[98:101], v[50:65]
	v_fma_f32 v44, v116, s34, v70
	v_fma_f32 v45, v117, s35, v70
	v_fma_f32 v42, v116, s80, v70
	v_fma_f32 v43, v117, s81, v70
	v_fma_f32 v40, v116, s76, v70
	v_fma_f32 v41, v117, s77, v70
	v_pk_fma_f32 v[38:39], v[116:117], s[82:83], v[70:71] op_sel_hi:[1,1,0]
	v_pk_fma_f32 v[36:37], v[116:117], s[84:85], v[70:71] op_sel_hi:[1,1,0]
	v_pk_fma_f32 v[34:35], v[120:121], s[86:87], v[70:71] op_sel_hi:[1,1,0]
	v_add3_u32 v70, s58, v71, v75
	v_sub_u32_e32 v96, v0, v95
	s_waitcnt lgkmcnt(0)
	v_mfma_f32_32x32x16_bf16 v[34:49], v[66:69], v[98:101], v[34:49]
	ds_read_b128 v[66:69], v70
	ds_read_b128 v[70:73], v70 offset:4096
	s_waitcnt lgkmcnt(1)
	v_mfma_f32_32x32x16_bf16 v[50:65], v[66:69], v[102:105], v[50:65]
	v_add_u32_e32 v66, 4, v74
	v_bitop3_b32 v66, v66, v94, 7 bitop3:0x78
	v_lshlrev_b32_e32 v66, 4, v66
	s_waitcnt lgkmcnt(0)
	v_mfma_f32_32x32x16_bf16 v[34:49], v[70:73], v[102:105], v[34:49]
	v_add3_u32 v70, s58, v66, v75
	ds_read_b128 v[66:69], v70
	ds_read_b128 v[70:73], v70 offset:4096
	s_waitcnt lgkmcnt(1)
	v_mfma_f32_32x32x16_bf16 v[50:65], v[66:69], v[106:109], v[50:65]
	v_add_u32_e32 v66, 6, v74
	v_bitop3_b32 v66, v66, v94, 7 bitop3:0x78
	v_lshlrev_b32_e32 v66, 4, v66
	s_waitcnt lgkmcnt(0)
	v_mfma_f32_32x32x16_bf16 v[34:49], v[70:73], v[106:109], v[34:49]
	v_add3_u32 v70, s58, v66, v75
	ds_read_b128 v[66:69], v70
	ds_read_b128 v[70:73], v70 offset:4096
	s_waitcnt lgkmcnt(1)
	v_mfma_f32_32x32x16_bf16 v[50:65], v[66:69], v[110:113], v[50:65]
	v_add_u32_e32 v67, 0x200, v96
	v_cmp_gt_u32_e32 vcc, s15, v67
	v_add_u32_e32 v66, 0x200, v0
	v_or_b32_e32 v67, 2, v95
	s_waitcnt lgkmcnt(0)
	v_mfma_f32_32x32x16_bf16 v[34:49], v[70:73], v[110:113], v[34:49]
	s_nop 5
	v_cndmask_b32_e32 v133, v233, v50, vcc
	v_add_u32_e32 v50, 0x1ff, v96
	v_cmp_gt_u32_e32 vcc, s15, v50
	v_or_b32_e32 v50, 3, v95
	s_nop 0
	v_cndmask_b32_e32 v117, v233, v51, vcc
	v_sub_u32_e32 v51, v66, v50
	v_sub_u32_e32 v50, v66, v67
	v_cmp_gt_u32_e32 vcc, s15, v51
	v_add_u32_e32 v67, 0x1f8, v96
	s_nop 0
	v_cndmask_b32_e32 v93, v233, v53, vcc
	v_cmp_gt_u32_e32 vcc, s15, v50
	v_add_u32_e32 v53, 0x1f7, v96
	v_pk_mov_b32 v[50:51], v[50:51], v[50:51] op_sel:[1,0]
	v_cndmask_b32_e32 v92, v233, v52, vcc
	v_add_u32_e32 v52, 8, v95
	v_cmp_gt_u32_e32 vcc, s15, v53
	v_or_b32_e32 v53, 3, v52
	v_or_b32_e32 v52, 2, v52
	v_cndmask_b32_e32 v91, v233, v55, vcc
	v_cmp_gt_u32_e32 vcc, s15, v67
	v_sub_u32_e32 v53, v66, v53
	v_sub_u32_e32 v52, v66, v52
	v_cndmask_b32_e32 v90, v233, v54, vcc
	v_cmp_gt_u32_e32 vcc, s15, v53
	v_add_u32_e32 v54, 16, v95
	v_add_u32_e32 v55, 0x1ef, v96
	v_cndmask_b32_e32 v89, v233, v57, vcc
	v_cmp_gt_u32_e32 vcc, s15, v52
	v_add_u32_e32 v57, 0x1e7, v96
	s_nop 0
	v_cndmask_b32_e32 v88, v233, v56, vcc
	v_add_u32_e32 v56, 0x1f0, v96
	v_cmp_gt_u32_e32 vcc, s15, v55
	v_or_b32_e32 v55, 3, v54
	v_or_b32_e32 v54, 2, v54
	v_cndmask_b32_e32 v87, v233, v59, vcc
	v_cmp_gt_u32_e32 vcc, s15, v56
	v_sub_u32_e32 v55, v66, v55
	v_sub_u32_e32 v54, v66, v54
	v_cndmask_b32_e32 v86, v233, v58, vcc
	v_cmp_gt_u32_e32 vcc, s15, v55
	v_add_u32_e32 v56, 24, v95
	v_add_u32_e32 v58, 0x1e8, v96
	v_cndmask_b32_e32 v85, v233, v61, vcc
	v_cmp_gt_u32_e32 vcc, s15, v54
	s_nop 1
	v_cndmask_b32_e32 v84, v233, v60, vcc
	v_cmp_gt_u32_e32 vcc, s15, v57
	v_or_b32_e32 v57, 3, v56
	v_or_b32_e32 v56, 2, v56
	v_cndmask_b32_e32 v83, v233, v63, vcc
	v_cmp_gt_u32_e32 vcc, s15, v58
	v_sub_u32_e32 v57, v66, v57
	v_sub_u32_e32 v56, v66, v56
	v_cndmask_b32_e32 v82, v233, v62, vcc
	v_cmp_gt_u32_e32 vcc, s15, v57
	v_add_u32_e32 v58, 0x1e0, v96
	s_nop 0
	v_cndmask_b32_e32 v81, v233, v65, vcc
	v_cmp_gt_u32_e32 vcc, s15, v56
	s_nop 1
	v_cndmask_b32_e32 v80, v233, v64, vcc
	v_cmp_gt_u32_e32 vcc, s15, v58
	s_nop 1
	v_cndmask_b32_e32 v97, v233, v34, vcc
	v_subrev_u32_e32 v34, 32, v51
	v_add_u32_e32 v51, 0x1df, v96
	v_cmp_gt_u32_e32 vcc, s15, v34
	v_subrev_u32_e32 v34, 32, v50
	s_nop 0
	v_cndmask_b32_e32 v79, v233, v36, vcc
	v_cmp_gt_u32_e32 vcc, s15, v51
	v_add_u32_e32 v36, 0x1d7, v96
	s_nop 0
	v_cndmask_b32_e32 v78, v233, v35, vcc
	v_add_u32_e32 v35, 0x1d8, v96
	v_cmp_gt_u32_e32 vcc, s15, v35
	s_nop 1
	v_cndmask_b32_e32 v77, v233, v38, vcc
; template <int MODE, int MK  , bool FIRST, class ValidF> ...
;     ...
;     if (MK != 0) {
; #pragma unroll
;         for (int mt = 0; mt < 2; ++mt)
; #pragma unroll
;             for (int r = 0; r < 16; ++r) { const int kc = 32 * mt + (r & 3) + 8 * (r >> 2); const bool ok = (MK == 2) ? valid(kc + 4 * hh) : lv; p[mt][r] = ok ? p[mt][r] : -INFINITY; } }
;     if (MODE != 1) {
;         float tmax = fmaxf(p[0][0], p[1][0]);
; #pragma unroll
;         for (int r = 1; r < 16; ++r) tmax = fmaxf(tmax, fmaxf(p[0][r], p[1][r]));
;         tmax = fmaxf(tmax, __shfl_xor(tmax, 32));
;         if (MODE == 0) {
;             const float mn = fmaxf(m, tmax); const float mm = (mn == -INFINITY) ? 0.f : mn; l *= __builtin_amdgcn_exp2f(m - mm); m = mn;
; #pragma unroll
;             for (int mt = 0; mt < 2; ++mt)
; #pragma unroll
;                 for (int r = 0; r < 16; ++r) p[mt][r] -= mm;
;         } else if (FIRST) {
;             m = tmax;
; #pragma unroll
;             for (int mt = 0; mt < 2; ++mt)
; #pragma unroll
;                 for (int r = 0; r < 16; ++r) p[mt][r] -= tmax;
;         } else if (__any(tmax > 8.0f)) {
;             const float dl = fmaxf(tmax, 0.f); m += dl; const float f = __builtin_amdgcn_exp2f(-dl); l *= f;
; #pragma unroll
;             for (int mt = 0; mt < 2; ++mt)
; #pragma unroll
;                 for (int r = 0; r < 16; ++r) p[mt][r] -= dl;
; #pragma unroll
;             for (int i = 0; i < 16; ++i) { o[0][i] *= f; o[1][i] *= f; } }
	v_cmp_gt_u32_e32 vcc, s15, v34
	v_pk_mov_b32 v[34:35], v[52:53], v[52:53] op_sel:[1,0]
	s_nop 0
	v_subrev_u32_e32 v35, 32, v35
	v_cndmask_b32_e32 v76, v233, v37, vcc
	v_cmp_gt_u32_e32 vcc, s15, v35
	v_add_u32_e32 v35, 0x1d0, v96
	v_subrev_u32_e32 v34, 32, v34
	v_cndmask_b32_e32 v75, v233, v40, vcc
	v_cmp_gt_u32_e32 vcc, s15, v36
	v_add_u32_e32 v36, 0x1cf, v96
	v_max_f32_e32 v37, v93, v93
	v_cndmask_b32_e32 v74, v233, v39, vcc
	v_cmp_gt_u32_e32 vcc, s15, v35
	s_nop 1
	v_cndmask_b32_e32 v73, v233, v42, vcc
	v_cmp_gt_u32_e32 vcc, s15, v34
	v_pk_mov_b32 v[34:35], v[54:55], v[54:55] op_sel:[1,0]
	s_nop 0
	v_subrev_u32_e32 v35, 32, v35
	v_cndmask_b32_e32 v72, v233, v41, vcc
	v_cmp_gt_u32_e32 vcc, s15, v35
	v_add_u32_e32 v35, 0x1c8, v96
	v_subrev_u32_e32 v34, 32, v34
	v_cndmask_b32_e32 v69, v233, v44, vcc
	v_cmp_gt_u32_e32 vcc, s15, v36
	v_max_f32_e32 v36, v92, v92
	s_nop 0
	v_cndmask_b32_e32 v68, v233, v43, vcc
	v_cmp_gt_u32_e32 vcc, s15, v35
	v_add_u32_e32 v35, 0x1c7, v96
	s_nop 0
	v_cndmask_b32_e32 v67, v233, v46, vcc
	v_cmp_gt_u32_e32 vcc, s15, v34
	v_subrev_u32_e32 v34, 32, v56
	s_nop 0
	v_cndmask_b32_e32 v66, v233, v45, vcc
	v_cmp_gt_u32_e32 vcc, s15, v34
	v_subrev_u32_e32 v34, 32, v57
	s_nop 0
	v_cndmask_b32_e32 v71, v233, v48, vcc
	v_cmp_gt_u32_e32 vcc, s15, v35
	v_max_f32_e32 v35, v117, v117
	s_nop 0
	v_cndmask_b32_e32 v70, v233, v47, vcc
	v_cmp_gt_u32_e32 vcc, s15, v34
	v_max_f32_e32 v34, v78, v78
	v_max_f32_e32 v34, v35, v34
	v_max_f32_e32 v35, v79, v79
	v_max_f32_e32 v35, v36, v35
	v_max_f32_e32 v36, v76, v76
	v_max3_f32 v34, v133, v97, v34
	v_max_f32_e32 v36, v37, v36
	v_max3_f32 v34, v34, v35, v36
	v_max_f32_e32 v35, v77, v77
	v_max_f32_e32 v36, v90, v90
	v_max_f32_e32 v35, v36, v35
	v_max_f32_e32 v36, v74, v74
	v_max_f32_e32 v37, v91, v91
	v_max_f32_e32 v36, v37, v36
	v_max3_f32 v34, v34, v35, v36
	v_max_f32_e32 v35, v75, v75
	v_max_f32_e32 v36, v88, v88
	v_max_f32_e32 v35, v36, v35
	v_max_f32_e32 v36, v72, v72
	v_max_f32_e32 v37, v89, v89
	v_max_f32_e32 v36, v37, v36
	v_max3_f32 v34, v34, v35, v36
	v_max_f32_e32 v35, v73, v73
	v_max_f32_e32 v36, v86, v86
	v_max_f32_e32 v35, v36, v35
	v_max_f32_e32 v36, v68, v68
	v_max_f32_e32 v37, v87, v87
	v_max_f32_e32 v36, v37, v36
	v_max3_f32 v34, v34, v35, v36
	v_max_f32_e32 v35, v69, v69
	v_max_f32_e32 v36, v84, v84
	v_max_f32_e32 v35, v36, v35
	v_max_f32_e32 v36, v66, v66
	v_max_f32_e32 v37, v85, v85
	v_max_f32_e32 v36, v37, v36
	v_max3_f32 v34, v34, v35, v36
	v_max_f32_e32 v35, v67, v67
	v_max_f32_e32 v36, v82, v82
	v_max_f32_e32 v35, v36, v35
	v_max_f32_e32 v36, v70, v70
	v_max_f32_e32 v37, v83, v83
	v_max_f32_e32 v36, v37, v36
	v_cndmask_b32_e32 v96, v233, v49, vcc
	v_max3_f32 v34, v34, v35, v36
	v_max_f32_e32 v35, v71, v71
	v_max_f32_e32 v36, v80, v80
	v_max_f32_e32 v35, v36, v35
	v_max_f32_e32 v36, v96, v96
	v_max_f32_e32 v37, v81, v81
	v_max_f32_e32 v36, v37, v36
	v_max3_f32 v34, v34, v35, v36
	v_mov_b32_e32 v35, v34
	s_nop 1
	v_permlane32_swap_b32_e32 v34, v35
	s_waitcnt lgkmcnt(0)
	v_max_f32_e32 v35, v35, v35
	v_max_f32_e32 v34, v34, v35
	v_cmp_lt_f32_e32 vcc, s74, v34
	s_cbranch_vccz .LBB0_569
	v_max_f32_e32 v34, v34, v34
	v_max_f32_e32 v34, 0, v34
	v_exp_f32_e64 v136, -v34
	v_add_f32_e32 v132, v132, v34
	v_sub_f32_e32 v133, v133, v34
	v_sub_f32_e32 v117, v117, v34
	v_mul_f32_e32 v134, v131, v136
	v_pk_add_f32 v[92:93], v[92:93], v[34:35] op_sel_hi:[1,0] neg_lo:[0,1] neg_hi:[0,1]
	v_pk_add_f32 v[90:91], v[90:91], v[34:35] op_sel_hi:[1,0] neg_lo:[0,1] neg_hi:[0,1]
	v_pk_add_f32 v[88:89], v[88:89], v[34:35] op_sel_hi:[1,0] neg_lo:[0,1] neg_hi:[0,1]
	v_pk_add_f32 v[86:87], v[86:87], v[34:35] op_sel_hi:[1,0] neg_lo:[0,1] neg_hi:[0,1]
	v_pk_add_f32 v[84:85], v[84:85], v[34:35] op_sel_hi:[1,0] neg_lo:[0,1] neg_hi:[0,1]
	v_pk_add_f32 v[82:83], v[82:83], v[34:35] op_sel_hi:[1,0] neg_lo:[0,1] neg_hi:[0,1]
	v_pk_add_f32 v[80:81], v[80:81], v[34:35] op_sel_hi:[1,0] neg_lo:[0,1] neg_hi:[0,1]
	v_sub_f32_e32 v97, v97, v34
	v_pk_add_f32 v[78:79], v[78:79], v[34:35] op_sel_hi:[1,0] neg_lo:[0,1] neg_hi:[0,1]
	v_pk_add_f32 v[76:77], v[76:77], v[34:35] op_sel_hi:[1,0] neg_lo:[0,1] neg_hi:[0,1]
	v_pk_add_f32 v[74:75], v[74:75], v[34:35] op_sel_hi:[1,0] neg_lo:[0,1] neg_hi:[0,1]
	v_pk_add_f32 v[72:73], v[72:73], v[34:35] op_sel_hi:[1,0] neg_lo:[0,1] neg_hi:[0,1]
	v_pk_add_f32 v[68:69], v[68:69], v[34:35] op_sel_hi:[1,0] neg_lo:[0,1] neg_hi:[0,1]
	v_pk_add_f32 v[66:67], v[66:67], v[34:35] op_sel_hi:[1,0] neg_lo:[0,1] neg_hi:[0,1]
	v_pk_add_f32 v[70:71], v[70:71], v[34:35] op_sel_hi:[1,0] neg_lo:[0,1] neg_hi:[0,1]
	v_sub_f32_e32 v96, v96, v34
	v_pk_mul_f32 v[64:65], v[32:33], v[136:137] op_sel_hi:[1,0]
	v_pk_mul_f32 v[62:63], v[30:31], v[136:137] op_sel_hi:[1,0]
	v_pk_mul_f32 v[60:61], v[28:29], v[136:137] op_sel_hi:[1,0]
	v_pk_mul_f32 v[58:59], v[26:27], v[136:137] op_sel_hi:[1,0]
	v_pk_mul_f32 v[56:57], v[24:25], v[136:137] op_sel_hi:[1,0]
	v_pk_mul_f32 v[54:55], v[22:23], v[136:137] op_sel_hi:[1,0]
	v_pk_mul_f32 v[52:53], v[20:21], v[136:137] op_sel_hi:[1,0]
	v_pk_mul_f32 v[50:51], v[18:19], v[136:137] op_sel_hi:[1,0]
	v_pk_mul_f32 v[48:49], v[16:17], v[136:137] op_sel_hi:[1,0]
	v_pk_mul_f32 v[46:47], v[14:15], v[136:137] op_sel_hi:[1,0]
	v_pk_mul_f32 v[44:45], v[12:13], v[136:137] op_sel_hi:[1,0]
	v_pk_mul_f32 v[42:43], v[10:11], v[136:137] op_sel_hi:[1,0]
	v_pk_mul_f32 v[40:41], v[8:9], v[136:137] op_sel_hi:[1,0]
	v_pk_mul_f32 v[38:39], v[6:7], v[136:137] op_sel_hi:[1,0]
	v_pk_mul_f32 v[36:37], v[4:5], v[136:137] op_sel_hi:[1,0]
	v_pk_mul_f32 v[34:35], v[2:3], v[136:137] op_sel_hi:[1,0]
	s_branch .LBB0_570

; #define LAS __attribute__((address_space(3)))
; #define MFMA32(a, b, c) __builtin_amdgcn_mfma_f32_32x32x16_bf16((a), (b), (c), 0, 0, 0)
; template <int MODE, int MK  , bool FIRST, class ValidF> ...
;     ...
;     const float cref = c0 + sbk * (float)(4 * hh) - ((MODE == 2 && !FIRST) || MODE == 1 ? m : 0.f);
; #pragma unroll
;     for (int mt = 0; mt < 2; ++mt)
; #pragma unroll
;         for (int r = 0; r < 16; ++r) p[mt][r] = fmaf(sbk, (float)(32 * mt + (r & 3) + 8 * (r >> 2)), cref);
; #pragma unroll
;     for (int ks = 0; ks < 4; ++ks)
; #pragma unroll
;         for (int mt = 0; mt < 2; ++mt) { const bf16x8 a = *(const LAS bf16x8*)(Kb + kofs[ks] + mt * 4096); p[mt] = MFMA32(a, qf[ks], p[mt]); }
;     if (MK != 0) {
; #pragma unroll
;         for (int mt = 0; mt < 2; ++mt)
; #pragma unroll
;             for (int r = 0; r < 16; ++r) { const int kc = 32 * mt + (r & 3) + 8 * (r >> 2); const bool ok = (MK == 2) ? valid(kc + 4 * hh) : lv; p[mt][r] = ok ? p[mt][r] : -INFINITY; } }
; __device__ __forceinline__ void nsa_mfma_phase(Frame& F, int l, bf16* YC, int ypitch) {
;     ...
;                     auto valid = [&](int koff) { return (dj + tq - koff >= 0) && (dj + tq - koff <= WIN - 1); };
;                     const LAS unsigned char* Kb = lds + L_K + slot * TB; const LAS unsigned char* Vb = lds + L_V + slot * TB;
;                     if (j == c) tile_compute<2, 2, true>(Kb, Vb, qf, slope2 * (float)(64 * (j - c)), slope2, true, valid, m, lsum, o, IMP, L);
.LBB0_568:
	v_mov_b32_e32 v71, v123
	v_mov_b32_e32 v117, v116
	v_ashrrev_i32_e32 v34, 5, v71
	v_lshlrev_b32_e32 v35, 7, v71
	v_and_b32_e32 v72, 0xf80, v35
	v_bitop3_b32 v35, v34, v71, 7 bitop3:0x78
	s_nop 3
	v_lshlrev_b32_e32 v50, 4, v35
	v_add_u32_e32 v35, 2, v34
	v_add3_u32 v54, s58, v50, v72
	v_bitop3_b32 v35, v35, v71, 7 bitop3:0x78
	ds_read_b128 v[50:53], v54
	ds_read_b128 v[66:69], v54 offset:4096
	v_lshlrev_b32_e32 v73, 4, v35
	v_add_u32_e32 v35, 4, v34
	v_bitop3_b32 v35, v35, v71, 7 bitop3:0x78
	v_lshlrev_b32_e32 v76, 2, v34
	v_lshlrev_b32_e32 v74, 4, v35
	v_add_u32_e32 v35, 6, v34
	v_cvt_f32_i32_e32 v34, v76
	v_bitop3_b32 v35, v35, v71, 7 bitop3:0x78
	v_lshlrev_b32_e32 v75, 4, v35
	v_sub_u32_e32 v0, v0, v76
	v_fma_f32 v70, v116, v34, v129
	v_fma_f32 v34, 0, v116, v70
	v_add_f32_e32 v35, v116, v70
	v_pk_fma_f32 v[36:37], v[118:119], s[18:19], v[70:71] op_sel_hi:[1,1,0]
	v_pk_fma_f32 v[38:39], v[118:119], s[74:75], v[70:71] op_sel_hi:[1,1,0]
	v_pk_fma_f32 v[40:41], v[118:119], s[36:37], v[70:71] op_sel_hi:[1,1,0]
	v_pk_fma_f32 v[42:43], v[118:119], s[26:27], v[70:71] op_sel_hi:[1,1,0]
	v_pk_fma_f32 v[44:45], v[118:119], s[56:57], v[70:71] op_sel_hi:[1,1,0]
	v_pk_fma_f32 v[46:47], v[118:119], s[22:23], v[70:71] op_sel_hi:[1,1,0]
	v_pk_fma_f32 v[48:49], v[118:119], s[24:25], v[70:71] op_sel_hi:[1,1,0]
	v_pk_fma_f32 v[64:65], v[116:117], s[30:31], v[70:71] op_sel_hi:[1,1,0]
	v_pk_fma_f32 v[62:63], v[116:117], s[20:21], v[70:71] op_sel_hi:[1,1,0]
	s_waitcnt lgkmcnt(1)
	v_mfma_f32_32x32x16_bf16 v[34:49], v[50:53], v[98:101], v[34:49]
	v_fma_f32 v60, v116, s34, v70
	v_fma_f32 v61, v117, s35, v70
	v_fma_f32 v58, v116, s80, v70
	v_fma_f32 v59, v117, s81, v70
	v_fma_f32 v56, v116, s76, v70
	v_fma_f32 v57, v117, s77, v70
	v_pk_fma_f32 v[54:55], v[116:117], s[82:83], v[70:71] op_sel_hi:[1,1,0]
	v_pk_fma_f32 v[52:53], v[116:117], s[84:85], v[70:71] op_sel_hi:[1,1,0]
	v_pk_fma_f32 v[50:51], v[120:121], s[86:87], v[70:71] op_sel_hi:[1,1,0]
	v_add3_u32 v70, s58, v73, v72
	v_cmp_gt_u32_e32 vcc, s15, v0
	s_waitcnt lgkmcnt(0)
	v_mfma_f32_32x32x16_bf16 v[50:65], v[66:69], v[98:101], v[50:65]
	ds_read_b128 v[66:69], v70
	s_waitcnt lgkmcnt(0)
	v_mfma_f32_32x32x16_bf16 v[34:49], v[66:69], v[102:105], v[34:49]
	ds_read_b128 v[66:69], v70 offset:4096
	v_add3_u32 v70, s58, v74, v72
	s_waitcnt lgkmcnt(0)
	v_mfma_f32_32x32x16_bf16 v[50:65], v[66:69], v[102:105], v[50:65]
	ds_read_b128 v[66:69], v70
	s_waitcnt lgkmcnt(0)
	v_mfma_f32_32x32x16_bf16 v[34:49], v[66:69], v[106:109], v[34:49]
	ds_read_b128 v[66:69], v70 offset:4096
	v_add3_u32 v70, s58, v75, v72
	s_waitcnt lgkmcnt(0)
	v_mfma_f32_32x32x16_bf16 v[50:65], v[66:69], v[106:109], v[50:65]
	ds_read_b128 v[66:69], v70
	s_waitcnt lgkmcnt(0)
	v_mfma_f32_32x32x16_bf16 v[34:49], v[66:69], v[110:113], v[34:49]
	ds_read_b128 v[66:69], v70 offset:4096
	s_waitcnt lgkmcnt(0)
	v_mfma_f32_32x32x16_bf16 v[50:65], v[66:69], v[110:113], v[50:65]
	v_add_u32_e32 v67, -1, v0
	s_nop 7
	v_cndmask_b32_e32 v34, v233, v34, vcc
	v_cmp_gt_u32_e32 vcc, s15, v67
	v_add_u32_e32 v67, -2, v0
	v_subrev_u32_e32 v66, 59, v0
	v_cndmask_b32_e32 v35, v233, v35, vcc
	v_cmp_gt_u32_e32 vcc, s15, v67
	v_add_u32_e32 v67, -3, v0
	v_bfe_u32 v68, v71, 1, 1
	v_cndmask_b32_e32 v36, v233, v36, vcc
	v_cmp_gt_u32_e32 vcc, s15, v67
	v_add_u32_e32 v67, -8, v0
	v_max_f32_e32 v70, v36, v36
	v_cndmask_b32_e32 v37, v233, v37, vcc
	v_cmp_gt_u32_e32 vcc, s15, v67
	v_add_u32_e32 v67, -9, v0
	s_nop 0
	v_cndmask_b32_e32 v38, v233, v38, vcc
	v_cmp_gt_u32_e32 vcc, s15, v67
	v_add_u32_e32 v67, -10, v0
	s_nop 0
	v_cndmask_b32_e32 v39, v233, v39, vcc
	v_cmp_gt_u32_e32 vcc, s15, v67
	v_add_u32_e32 v67, -11, v0
	s_nop 0
	v_cndmask_b32_e32 v40, v233, v40, vcc
	v_cmp_gt_u32_e32 vcc, s15, v67
	v_add_u32_e32 v67, -16, v0
	s_nop 0
	v_cndmask_b32_e32 v41, v233, v41, vcc
	v_cmp_gt_u32_e32 vcc, s15, v67
	v_subrev_u32_e32 v67, 17, v0
	s_nop 0
	v_cndmask_b32_e32 v42, v233, v42, vcc
	v_cmp_gt_u32_e32 vcc, s15, v67
	v_subrev_u32_e32 v67, 18, v0
	s_nop 0
	v_cndmask_b32_e32 v43, v233, v43, vcc
	v_cmp_gt_u32_e32 vcc, s15, v67
	v_subrev_u32_e32 v67, 19, v0
	s_nop 0
	v_cndmask_b32_e32 v44, v233, v44, vcc
	v_cmp_gt_u32_e32 vcc, s15, v67
	v_subrev_u32_e32 v67, 24, v0
	s_nop 0
	v_cndmask_b32_e32 v45, v233, v45, vcc
	v_cmp_gt_u32_e32 vcc, s15, v67
	v_subrev_u32_e32 v67, 25, v0
	s_nop 0
	v_cndmask_b32_e32 v46, v233, v46, vcc
	v_cmp_gt_u32_e32 vcc, s15, v67
	v_subrev_u32_e32 v67, 26, v0
	s_nop 0
	v_cndmask_b32_e32 v47, v233, v47, vcc
	v_cmp_gt_u32_e32 vcc, s15, v67
	v_subrev_u32_e32 v67, 27, v0
	s_nop 0
	v_cndmask_b32_e32 v48, v233, v48, vcc
	v_cmp_gt_u32_e32 vcc, s15, v67
	v_subrev_u32_e32 v67, 32, v0
	s_nop 0
	v_cndmask_b32_e32 v49, v233, v49, vcc
	v_cmp_gt_u32_e32 vcc, s15, v67
	s_nop 1
	v_cndmask_b32_e32 v67, v233, v50, vcc
	v_subrev_u32_e32 v50, 33, v0
	v_cmp_gt_u32_e32 vcc, s15, v50
	v_subrev_u32_e32 v50, 34, v0
	s_nop 0
	v_cndmask_b32_e32 v51, v233, v51, vcc
	v_cmp_gt_u32_e32 vcc, s15, v50
	v_subrev_u32_e32 v50, 35, v0
	s_nop 0
	v_cndmask_b32_e32 v52, v233, v52, vcc
	v_cmp_gt_u32_e32 vcc, s15, v50
	v_subrev_u32_e32 v50, 40, v0
	s_nop 0
	v_cndmask_b32_e32 v53, v233, v53, vcc
	v_cmp_gt_u32_e32 vcc, s15, v50
	v_subrev_u32_e32 v50, 41, v0
	s_nop 0
	v_cndmask_b32_e32 v54, v233, v54, vcc
	v_cmp_gt_u32_e32 vcc, s15, v50
	v_subrev_u32_e32 v50, 42, v0
	s_nop 0
	v_cndmask_b32_e32 v55, v233, v55, vcc
	v_cmp_gt_u32_e32 vcc, s15, v50
	v_subrev_u32_e32 v50, 43, v0
	s_nop 0
	v_cndmask_b32_e32 v56, v233, v56, vcc
	v_cmp_gt_u32_e32 vcc, s15, v50
	v_subrev_u32_e32 v50, 48, v0
	s_nop 0
	v_cndmask_b32_e32 v57, v233, v57, vcc
	v_cmp_gt_u32_e32 vcc, s15, v50
	v_subrev_u32_e32 v50, 49, v0
	s_nop 0
; template <int MODE, int MK  , bool FIRST, class ValidF> ...
;     ...
;     if (MK != 0) {
; #pragma unroll
;         for (int mt = 0; mt < 2; ++mt)
; #pragma unroll
;             for (int r = 0; r < 16; ++r) { const int kc = 32 * mt + (r & 3) + 8 * (r >> 2); const bool ok = (MK == 2) ? valid(kc + 4 * hh) : lv; p[mt][r] = ok ? p[mt][r] : -INFINITY; } }
;     if (MODE != 1) {
;         float tmax = fmaxf(p[0][0], p[1][0]);
; #pragma unroll
;         for (int r = 1; r < 16; ++r) tmax = fmaxf(tmax, fmaxf(p[0][r], p[1][r]));
;         tmax = fmaxf(tmax, __shfl_xor(tmax, 32));
	v_cndmask_b32_e32 v58, v233, v58, vcc
	v_cmp_gt_u32_e32 vcc, s15, v50
	v_subrev_u32_e32 v50, 50, v0
	s_nop 0
	v_cndmask_b32_e32 v59, v233, v59, vcc
	v_cmp_gt_u32_e32 vcc, s15, v50
	v_subrev_u32_e32 v50, 51, v0
	s_nop 0
	v_cndmask_b32_e32 v60, v233, v60, vcc
	v_cmp_gt_u32_e32 vcc, s15, v50
	v_subrev_u32_e32 v50, 56, v0
	s_nop 0
	v_cndmask_b32_e32 v61, v233, v61, vcc
	v_cmp_gt_u32_e32 vcc, s15, v50
	v_subrev_u32_e32 v50, 57, v0
	v_subrev_u32_e32 v0, 58, v0
	v_cndmask_b32_e32 v62, v233, v62, vcc
	v_cmp_gt_u32_e32 vcc, s15, v50
	v_lshrrev_b32_e32 v50, 2, v71
	v_and_or_b32 v69, v50, 3, v76
	v_cndmask_b32_e32 v63, v233, v63, vcc
	v_cmp_gt_u32_e32 vcc, s15, v0
	v_lshrrev_b32_e32 v0, 3, v71
	v_lshlrev_b32_e32 v50, 3, v71
	v_cndmask_b32_e32 v64, v233, v64, vcc
	v_cmp_gt_u32_e32 vcc, s15, v66
	v_and_b32_e32 v66, 2, v0
	v_or_b32_e32 v0, v66, v68
	v_and_b32_e32 v50, 8, v50
	v_bitop3_b32 v0, v0, v69, 4 bitop3:0x36
	v_lshl_or_b32 v50, v69, 7, v50
	v_bitop3_b32 v66, v66, v69, v68 bitop3:0x36
	v_max_f32_e32 v68, v51, v51
	v_max_f32_e32 v69, v35, v35
	v_max_f32_e32 v68, v69, v68
	v_max_f32_e32 v69, v52, v52
	v_max_f32_e32 v69, v70, v69
	v_max_f32_e32 v70, v53, v53
	v_max_f32_e32 v71, v37, v37
	v_max3_f32 v68, v34, v67, v68
	v_max_f32_e32 v70, v71, v70
	v_max3_f32 v68, v68, v69, v70
	v_max_f32_e32 v69, v54, v54
	v_max_f32_e32 v70, v38, v38
	v_max_f32_e32 v69, v70, v69
	v_max_f32_e32 v70, v55, v55
	v_max_f32_e32 v71, v39, v39
	v_max_f32_e32 v70, v71, v70
	v_max3_f32 v68, v68, v69, v70
	v_max_f32_e32 v69, v56, v56
	v_max_f32_e32 v70, v40, v40
	v_max_f32_e32 v69, v70, v69
	v_max_f32_e32 v70, v57, v57
	v_max_f32_e32 v71, v41, v41
	v_max_f32_e32 v70, v71, v70
	v_max3_f32 v68, v68, v69, v70
	v_max_f32_e32 v69, v58, v58
	v_max_f32_e32 v70, v42, v42
	v_max_f32_e32 v69, v70, v69
	v_max_f32_e32 v70, v59, v59
	v_max_f32_e32 v71, v43, v43
	v_max_f32_e32 v70, v71, v70
	v_max3_f32 v68, v68, v69, v70
	v_max_f32_e32 v69, v60, v60
	v_max_f32_e32 v70, v44, v44
	v_max_f32_e32 v69, v70, v69
	v_max_f32_e32 v70, v61, v61
	v_max_f32_e32 v71, v45, v45
	v_max_f32_e32 v70, v71, v70
	v_max3_f32 v68, v68, v69, v70
	v_max_f32_e32 v69, v62, v62
	v_max_f32_e32 v70, v46, v46
	v_max_f32_e32 v69, v70, v69
	v_max_f32_e32 v70, v63, v63
	v_max_f32_e32 v71, v47, v47
	v_max_f32_e32 v70, v71, v70
	v_cndmask_b32_e32 v65, v233, v65, vcc
	v_max3_f32 v68, v68, v69, v70
	v_max_f32_e32 v69, v64, v64
	v_max_f32_e32 v70, v48, v48
	v_max_f32_e32 v69, v70, v69
	v_max_f32_e32 v70, v65, v65
	v_max_f32_e32 v71, v49, v49
	v_max_f32_e32 v70, v71, v70
	v_max3_f32 v68, v68, v69, v70
	v_mov_b32_e32 v69, v68
	s_nop 1
	v_permlane32_swap_b32_e32 v68, v69
	v_lshlrev_b32_e32 v66, 4, v66
	v_lshlrev_b32_e32 v0, 4, v0
	v_add3_u32 v0, s58, v0, v50
	s_waitcnt lgkmcnt(0)
; #define LAS __attribute__((address_space(3)))
; template <int MODE, int MK  , bool FIRST, class ValidF> ...
;     ...
;         } else if (FIRST) {
;             m = tmax;
; #pragma unroll
;             for (int mt = 0; mt < 2; ++mt)
; #pragma unroll
;                 for (int r = 0; r < 16; ++r) p[mt][r] -= tmax;
;         } else if (__any(tmax > 8.0f)) {
;             const float dl = fmaxf(tmax, 0.f); m += dl; const float f = __builtin_amdgcn_exp2f(-dl); l *= f;
; #pragma unroll
;             for (int mt = 0; mt < 2; ++mt)
; #pragma unroll
;                 for (int r = 0; r < 16; ++r) p[mt][r] -= dl;
; #pragma unroll
;             for (int i = 0; i < 16; ++i) { o[0][i] *= f; o[1][i] *= f; } }
;     }
;     float ls = 0.f;
; #pragma unroll
;     for (int mt = 0; mt < 2; ++mt)
; #pragma unroll
;         for (int r = 0; r < 16; ++r) { const float e = __builtin_amdgcn_exp2f(p[mt][r]); p[mt][r] = e; ls += e; }
;     l += ls;
;     if (MODE == 0) return;
;     if (MODE == 1) {
;         float av[8], bv[8];
; #pragma unroll
;         for (int mt = 0; mt < 2; ++mt)
; #pragma unroll
;             for (int g4 = 0; g4 < 4; ++g4) { const float h3 = 0.5f * p[mt][4 * g4 + 3]; av[mt * 4 + g4] = (p[mt][4 * g4] + p[mt][4 * g4 + 1]) + (p[mt][4 * g4 + 2] + h3); bv[mt * 4 + g4] = h3; }
; #pragma unroll
;         for (int i = 0; i < 8; ++i) imp[8 * (i >> 2) + 2 * (i & 3) + hh] += av[i];
;         asm volatile("s_waitcnt lgkmcnt(0)" ::: "memory"); __builtin_amdgcn_wave_barrier();
; #pragma unroll
;         for (int i = 0; i < 8; ++i) imp[8 * (i >> 2) + 2 * (i & 3) + hh + 1] += bv[i];
;         asm volatile("s_waitcnt lgkmcnt(0)" ::: "memory"); __builtin_amdgcn_wave_barrier();
;     }
;     bf16x8 pf[2][2];
; #pragma unroll
;     for (int mt = 0; mt < 2; ++mt)
; #pragma unroll
;         for (int sg = 0; sg < 2; ++sg) { u32x4 w; w.x = cvtpk(p[mt][8 * sg], p[mt][8 * sg + 1]); w.y = cvtpk(p[mt][8 * sg + 2], p[mt][8 * sg + 3]); w.z = cvtpk(p[mt][8 * sg + 4], p[mt][8 * sg + 5]); w.w = cvtpk(p[mt][8 * sg + 6], p[mt][8 * sg + 7]);
;             pf[mt][sg] = __builtin_bit_cast(bf16x8, w); }
; #pragma unroll
;     for (int dt = 0; dt < 2; ++dt)
; #pragma unroll
;         for (int mt = 0; mt < 2; ++mt)
; #pragma unroll
;             for (int sg = 0; sg < 2; ++sg) { const LAS unsigned char* vp = Vb + vofs[dt] + (32 * mt + 16 * sg) * 128;
	v_max_f32_e32 v69, v69, v69
	v_max_f32_e32 v117, v68, v69
	v_sub_f32_e32 v34, v34, v117
	v_sub_f32_e32 v35, v35, v117
	v_exp_f32_e32 v34, v34
	v_sub_f32_e32 v36, v36, v117
	v_exp_f32_e32 v35, v35
	v_sub_f32_e32 v37, v37, v117
	v_exp_f32_e32 v36, v36
	v_sub_f32_e32 v38, v38, v117
	v_exp_f32_e32 v37, v37
	v_sub_f32_e32 v39, v39, v117
	v_add_f32_e32 v68, 0, v34
	v_exp_f32_e32 v38, v38
	v_sub_f32_e32 v40, v40, v117
	v_add_f32_e32 v68, v35, v68
	v_exp_f32_e32 v39, v39
	v_sub_f32_e32 v41, v41, v117
	v_add_f32_e32 v68, v36, v68
	v_exp_f32_e32 v40, v40
	v_sub_f32_e32 v42, v42, v117
	v_add_f32_e32 v68, v37, v68
	v_exp_f32_e32 v41, v41
	v_sub_f32_e32 v43, v43, v117
	v_add_f32_e32 v68, v38, v68
	v_exp_f32_e32 v42, v42
	v_sub_f32_e32 v44, v44, v117
	v_add_f32_e32 v68, v39, v68
	v_exp_f32_e32 v43, v43
	v_sub_f32_e32 v45, v45, v117
	v_add_f32_e32 v68, v40, v68
	v_exp_f32_e32 v44, v44
	v_sub_f32_e32 v46, v46, v117
	v_add_f32_e32 v68, v41, v68
	v_exp_f32_e32 v45, v45
	v_add_f32_e32 v68, v42, v68
	v_exp_f32_e32 v69, v46
	v_add_f32_e32 v68, v43, v68
	v_add_f32_e32 v68, v44, v68
	v_sub_f32_e32 v47, v47, v117
	v_add_f32_e32 v68, v45, v68
	v_sub_f32_e32 v48, v48, v117
	v_add_f32_e32 v46, v69, v68
	v_exp_f32_e32 v68, v47
	v_sub_f32_e32 v49, v49, v117
	v_exp_f32_e32 v70, v48
	v_sub_f32_e32 v67, v67, v117
	v_exp_f32_e32 v71, v49
	v_sub_f32_e32 v51, v51, v117
	v_exp_f32_e32 v67, v67
	v_sub_f32_e32 v52, v52, v117
	v_add_f32_e32 v46, v68, v46
	v_exp_f32_e32 v51, v51
	v_sub_f32_e32 v53, v53, v117
	v_add_f32_e32 v46, v70, v46
	v_exp_f32_e32 v52, v52
	v_sub_f32_e32 v54, v54, v117
	v_add_f32_e32 v46, v71, v46
	v_exp_f32_e32 v53, v53
	v_sub_f32_e32 v55, v55, v117
	v_add_f32_e32 v46, v67, v46
	v_exp_f32_e32 v54, v54
	v_sub_f32_e32 v56, v56, v117
	v_add_f32_e32 v46, v51, v46
	v_exp_f32_e32 v55, v55
	v_sub_f32_e32 v57, v57, v117
	v_add_f32_e32 v46, v52, v46
	v_exp_f32_e32 v56, v56
	v_sub_f32_e32 v58, v58, v117
	v_add_f32_e32 v46, v53, v46
	v_exp_f32_e32 v57, v57
	v_sub_f32_e32 v59, v59, v117
	v_add_f32_e32 v46, v54, v46
	v_exp_f32_e32 v58, v58
	v_sub_f32_e32 v60, v60, v117
	v_add_f32_e32 v46, v55, v46
	v_exp_f32_e32 v59, v59
	v_sub_f32_e32 v61, v61, v117
	v_add_f32_e32 v46, v56, v46
	v_exp_f32_e32 v60, v60
	v_sub_f32_e32 v62, v62, v117
	v_add_f32_e32 v46, v57, v46
	v_exp_f32_e32 v61, v61
	v_sub_f32_e32 v63, v63, v117
	v_add_f32_e32 v46, v58, v46
	v_exp_f32_e32 v62, v62
	v_sub_f32_e32 v64, v64, v117
	v_add_f32_e32 v46, v59, v46
	v_exp_f32_e32 v63, v63
	v_sub_f32_e32 v65, v65, v117
	v_add_f32_e32 v46, v60, v46
	v_exp_f32_e32 v64, v64
	v_add_f32_e32 v46, v61, v46
	v_exp_f32_e32 v65, v65
	v_cvt_pk_bf16_f32 v48, v38, v39
	v_cvt_pk_bf16_f32 v38, v67, v51
	v_add3_u32 v51, s58, v66, v50
	v_add_f32_e32 v46, v62, v46
	v_cvt_pk_bf16_f32 v49, v40, v41
	v_cvt_pk_bf16_f32 v39, v52, v53
	v_cvt_pk_bf16_f32 v40, v54, v55
	ds_read_b64_tr_b16 v[52:53], v51 offset:24576
	ds_read_b64_tr_b16 v[54:55], v51 offset:25600
	v_add_f32_e32 v46, v63, v46
	v_add_f32_e32 v46, v64, v46
	v_add_f32_e32 v46, v65, v46
	v_add_f32_e32 v82, v131, v46
	v_cvt_pk_bf16_f32 v46, v34, v35
	v_cvt_pk_bf16_f32 v47, v36, v37
	v_cvt_pk_bf16_f32 v42, v42, v43
	v_cvt_pk_bf16_f32 v43, v44, v45
	s_waitcnt lgkmcnt(0)
	v_mfma_f32_32x32x16_bf16 v[2:17], v[52:55], v[46:49], v[2:17]
	ds_read_b64_tr_b16 v[52:53], v51 offset:26624
	ds_read_b64_tr_b16 v[54:55], v51 offset:27648
	v_cvt_pk_bf16_f32 v44, v69, v68
	v_cvt_pk_bf16_f32 v45, v70, v71
	v_cvt_pk_bf16_f32 v41, v56, v57
	v_cvt_pk_bf16_f32 v34, v58, v59
	v_cvt_pk_bf16_f32 v35, v60, v61
	v_cvt_pk_bf16_f32 v36, v62, v63
	s_waitcnt lgkmcnt(0)
	v_mfma_f32_32x32x16_bf16 v[2:17], v[52:55], v[42:45], v[2:17]
	ds_read_b64_tr_b16 v[52:53], v51 offset:28672
	ds_read_b64_tr_b16 v[54:55], v51 offset:29696
	v_cvt_pk_bf16_f32 v37, v64, v65
	s_waitcnt lgkmcnt(0)
	v_mfma_f32_32x32x16_bf16 v[2:17], v[52:55], v[38:41], v[2:17]
	ds_read_b64_tr_b16 v[52:53], v51 offset:30720
	ds_read_b64_tr_b16 v[54:55], v51 offset:31744
	s_waitcnt lgkmcnt(0)
	v_mfma_f32_32x32x16_bf16 v[2:17], v[52:55], v[34:37], v[2:17]
	ds_read_b64_tr_b16 v[50:51], v0 offset:24576
	ds_read_b64_tr_b16 v[52:53], v0 offset:25600
	s_waitcnt lgkmcnt(0)
	v_mfma_f32_32x32x16_bf16 v[18:33], v[50:53], v[46:49], v[18:33]
	ds_read_b64_tr_b16 v[46:47], v0 offset:26624
	ds_read_b64_tr_b16 v[48:49], v0 offset:27648
	s_waitcnt lgkmcnt(0)
	v_mfma_f32_32x32x16_bf16 v[18:33], v[46:49], v[42:45], v[18:33]
	ds_read_b64_tr_b16 v[42:43], v0 offset:28672
	ds_read_b64_tr_b16 v[44:45], v0 offset:29696
	s_waitcnt lgkmcnt(0)
	v_mfma_f32_32x32x16_bf16 v[18:33], v[42:45], v[38:41], v[18:33]
	ds_read_b64_tr_b16 v[38:39], v0 offset:30720
	ds_read_b64_tr_b16 v[40:41], v0 offset:31744
	s_waitcnt lgkmcnt(0)
	v_mfma_f32_32x32x16_bf16 v[18:33], v[38:41], v[34:37], v[18:33]
	s_nop 11
	v_mov_b64_e32 v[64:65], v[32:33]
	v_mov_b64_e32 v[62:63], v[30:31]
	v_mov_b64_e32 v[60:61], v[28:29]
	v_mov_b64_e32 v[58:59], v[26:27]
	v_mov_b64_e32 v[56:57], v[24:25]
	v_mov_b64_e32 v[54:55], v[22:23]
	v_mov_b64_e32 v[52:53], v[20:21]
	v_mov_b64_e32 v[50:51], v[18:19]
	v_mov_b64_e32 v[48:49], v[16:17]
	v_mov_b64_e32 v[46:47], v[14:15]
	v_mov_b64_e32 v[44:45], v[12:13]
	v_mov_b64_e32 v[42:43], v[10:11]
	v_mov_b64_e32 v[40:41], v[8:9]
	v_mov_b64_e32 v[38:39], v[6:7]
	v_mov_b64_e32 v[36:37], v[4:5]
	v_mov_b64_e32 v[34:35], v[2:3]
	s_branch .LBB0_547
